# routing phase rewritten: two tokens interleaved, DPP wave reductions replace serialized ds_bpermute chains; MLA loop pipelined (row max of next tile in PV block)
# speedup vs baseline: 1.0349x; 1.0349x over previous
; __device__ __forceinline__ float xhalf_max(float v) { auto rr = __builtin_amdgcn_permlane32_swap(__float_as_uint(v), __float_as_uint(v), false, false); return fmaxf(__uint_as_float(rr[0]), __uint_as_float(rr[1])); }
; template <bool ALIBI>
; __device__ __forceinline__ void attn_sv(const LAS unsigned char* kb, int vfo, f32x16& p0, f32x16& p1, float& m, float& l, f32x16& o0, f32x16& o1, int hi, int tq, int kpos0, float slope2, bool causal) {
;     ...
;     if (causal) {
; #pragma unroll
;         for (int r = 0; r < 16; ++r) { const int kv = krel + (r & 3) + 8 * (r >> 2); if (kv > 0) p0[r] = -INFINITY; if (kv + 32 > 0) p1[r] = -INFINITY; } }
;     float rm = fmaxf(p0[0], p1[0]);
; #pragma unroll
;     for (int r = 1; r < 16; ++r) rm = fmaxf(rm, fmaxf(p0[r], p1[r]));
;     rm = xhalf_max(rm);
;     const float mn = fmaxf(m, rm), alpha = __builtin_amdgcn_exp2f(m - mn);
.LBB0_774:
	s_nop 7
	s_nop 3
	s_cmp_lt_u32 s72, s77
	s_cbranch_scc1 .Lmla0_pre_nomask
	v_lshl_add_u32 v220, s72, 6, v201
	v_sub_u32_e32 v220, 0, v220
	v_cmp_gt_i32_e64 s[8:9], 0, v220
	v_cmp_gt_i32_e64 s[10:11], 1, v220
	v_cmp_gt_i32_e64 s[12:13], 2, v220
	v_cmp_gt_i32_e64 s[14:15], 3, v220
	v_cmp_gt_i32_e64 s[16:17], 8, v220
	v_cmp_gt_i32_e64 s[18:19], 9, v220
	v_cmp_gt_i32_e64 s[20:21], 10, v220
	v_cmp_gt_i32_e64 s[22:23], 11, v220
	v_cndmask_b32_e64 v18, v18, v1, s[8:9]
	v_cndmask_b32_e64 v19, v19, v1, s[10:11]
	v_cndmask_b32_e64 v20, v20, v1, s[12:13]
	v_cndmask_b32_e64 v21, v21, v1, s[14:15]
	v_cndmask_b32_e64 v22, v22, v1, s[16:17]
	v_cndmask_b32_e64 v23, v23, v1, s[18:19]
	v_cndmask_b32_e64 v24, v24, v1, s[20:21]
	v_cndmask_b32_e64 v25, v25, v1, s[22:23]
	v_cmp_gt_i32_e64 s[8:9], 16, v220
	v_cmp_gt_i32_e64 s[10:11], 17, v220
	v_cmp_gt_i32_e64 s[12:13], 18, v220
	v_cmp_gt_i32_e64 s[14:15], 19, v220
	v_cmp_gt_i32_e64 s[16:17], 24, v220
	v_cmp_gt_i32_e64 s[18:19], 25, v220
	v_cmp_gt_i32_e64 s[20:21], 26, v220
	v_cmp_gt_i32_e64 s[22:23], 27, v220
	v_cndmask_b32_e64 v26, v26, v1, s[8:9]
	v_cndmask_b32_e64 v27, v27, v1, s[10:11]
	v_cndmask_b32_e64 v28, v28, v1, s[12:13]
	v_cndmask_b32_e64 v29, v29, v1, s[14:15]
	v_cndmask_b32_e64 v30, v30, v1, s[16:17]
	v_cndmask_b32_e64 v31, v31, v1, s[18:19]
	v_cndmask_b32_e64 v32, v32, v1, s[20:21]
	v_cndmask_b32_e64 v33, v33, v1, s[22:23]
	v_cmp_gt_i32_e64 s[8:9], 32, v220
	v_cmp_gt_i32_e64 s[10:11], 33, v220
	v_cmp_gt_i32_e64 s[12:13], 34, v220
	v_cmp_gt_i32_e64 s[14:15], 35, v220
	v_cmp_gt_i32_e64 s[16:17], 40, v220
	v_cmp_gt_i32_e64 s[18:19], 41, v220
	v_cmp_gt_i32_e64 s[20:21], 42, v220
	v_cmp_gt_i32_e64 s[22:23], 43, v220
	v_cndmask_b32_e64 v2, v2, v1, s[8:9]
	v_cndmask_b32_e64 v3, v3, v1, s[10:11]
	v_cndmask_b32_e64 v4, v4, v1, s[12:13]
	v_cndmask_b32_e64 v5, v5, v1, s[14:15]
	v_cndmask_b32_e64 v6, v6, v1, s[16:17]
	v_cndmask_b32_e64 v7, v7, v1, s[18:19]
	v_cndmask_b32_e64 v8, v8, v1, s[20:21]
	v_cndmask_b32_e64 v9, v9, v1, s[22:23]
	v_cmp_gt_i32_e64 s[8:9], 48, v220
	v_cmp_gt_i32_e64 s[10:11], 49, v220
	v_cmp_gt_i32_e64 s[12:13], 50, v220
	v_cmp_gt_i32_e64 s[14:15], 51, v220
	v_cmp_gt_i32_e64 s[16:17], 56, v220
	v_cmp_gt_i32_e64 s[18:19], 57, v220
	v_cmp_gt_i32_e64 s[20:21], 58, v220
	v_cmp_gt_i32_e64 s[22:23], 59, v220
	v_cndmask_b32_e64 v10, v10, v1, s[8:9]
	v_cndmask_b32_e64 v11, v11, v1, s[10:11]
	v_cndmask_b32_e64 v12, v12, v1, s[12:13]
	v_cndmask_b32_e64 v13, v13, v1, s[14:15]
	v_cndmask_b32_e64 v14, v14, v1, s[16:17]
	v_cndmask_b32_e64 v15, v15, v1, s[18:19]
	v_cndmask_b32_e64 v16, v16, v1, s[20:21]
	v_cndmask_b32_e64 v17, v17, v1, s[22:23]
.Lmla0_pre_nomask:
	v_max3_f32 v218, v2, v3, v4
	v_max3_f32 v219, v18, v19, v20
	v_max3_f32 v218, v218, v5, v6
	v_max3_f32 v219, v219, v21, v22
	v_max3_f32 v218, v218, v7, v8
	v_max3_f32 v219, v219, v23, v24
	v_max3_f32 v218, v218, v9, v10
	v_max3_f32 v219, v219, v25, v26
	v_max3_f32 v218, v218, v11, v12
	v_max3_f32 v219, v219, v27, v28
	v_max3_f32 v218, v218, v13, v14
	v_max3_f32 v219, v219, v29, v30
	v_max3_f32 v218, v218, v15, v16
	v_max3_f32 v219, v219, v31, v32
	v_max3_f32 v218, v218, v17, v219
	v_max_f32_e32 v218, v218, v33
	v_mov_b32_e32 v219, v218
	s_nop 1
	v_permlane32_swap_b32_e32 v218, v219
	v_max3_f32 v214, v203, v218, v219
	v_sub_f32_e32 v218, v203, v214
	v_exp_f32_e32 v186, v218
	s_nop 0

; #define LAS __attribute__((address_space(3)))
; template <int DQK>
; __device__ __forceinline__ void attn_qk(const LAS unsigned char* kb, int kfo, const bf16x8 (&qf)[DQK / 16], f32x16& p0, f32x16& p1) {
;     constexpr int ND0 = DQK / 16;
;     bf16x8 ka[ND0], kc[ND0];
; #pragma unroll
;     for (int d0 = 0; d0 < ND0; ++d0) { ka[d0] = *(const LAS bf16x8*)(kb + kfo + d0 * 2048); kc[d0] = *(const LAS bf16x8*)(kb + kfo + d0 * 2048 + 512); }
;     __builtin_amdgcn_sched_barrier(0);
; #pragma unroll
;     for (int r = 0; r < 16; ++r) { p0[r] = 0.f; p1[r] = 0.f; }
; #pragma unroll
;     for (int d0 = 0; d0 < ND0; ++d0) {
;         p0 = __builtin_amdgcn_mfma_f32_32x32x16_bf16(ka[d0], qf[d0], p0, 0, 0, 0);
;         p1 = __builtin_amdgcn_mfma_f32_32x32x16_bf16(kc[d0], qf[d0], p1, 0, 0, 0);
;     }
; template <bool ALIBI>
; __device__ __forceinline__ void attn_sv(const LAS unsigned char* kb, int vfo, f32x16& p0, f32x16& p1, float& m, float& l, f32x16& o0, f32x16& o1, int hi, int tq, int kpos0, float slope2, bool causal) {
;     ...
;     float ls = 0.f;
; #pragma unroll
;     for (int r = 0; r < 16; ++r) { p0[r] = __builtin_amdgcn_exp2f(p0[r] - mn); p1[r] = __builtin_amdgcn_exp2f(p1[r] - mn); ls += p0[r] + p1[r]; }
;     l = l * alpha + ls;
; #pragma unroll
;     for (int r = 0; r < 16; ++r) { o0[r] *= alpha; o1[r] *= alpha; }
.Lmla0_h0_noiss:
	v_cmp_neq_f32_e32 vcc, 1.0, v186
	s_cbranch_vccz .Lmla0_h0_noresc
	v_pk_mul_f32 v[66:67], v[66:67], v[186:187] op_sel_hi:[1,0]
	v_pk_mul_f32 v[68:69], v[68:69], v[186:187] op_sel_hi:[1,0]
	v_pk_mul_f32 v[70:71], v[70:71], v[186:187] op_sel_hi:[1,0]
	v_pk_mul_f32 v[72:73], v[72:73], v[186:187] op_sel_hi:[1,0]
	v_pk_mul_f32 v[74:75], v[74:75], v[186:187] op_sel_hi:[1,0]
	v_pk_mul_f32 v[76:77], v[76:77], v[186:187] op_sel_hi:[1,0]
	v_pk_mul_f32 v[78:79], v[78:79], v[186:187] op_sel_hi:[1,0]
	v_pk_mul_f32 v[80:81], v[80:81], v[186:187] op_sel_hi:[1,0]
	v_pk_mul_f32 v[82:83], v[82:83], v[186:187] op_sel_hi:[1,0]
	v_pk_mul_f32 v[84:85], v[84:85], v[186:187] op_sel_hi:[1,0]
	v_pk_mul_f32 v[86:87], v[86:87], v[186:187] op_sel_hi:[1,0]
	v_pk_mul_f32 v[88:89], v[88:89], v[186:187] op_sel_hi:[1,0]
	v_pk_mul_f32 v[90:91], v[90:91], v[186:187] op_sel_hi:[1,0]
	v_pk_mul_f32 v[92:93], v[92:93], v[186:187] op_sel_hi:[1,0]
	v_pk_mul_f32 v[94:95], v[94:95], v[186:187] op_sel_hi:[1,0]
	v_pk_mul_f32 v[96:97], v[96:97], v[186:187] op_sel_hi:[1,0]
.Lmla0_h0_noresc:
	v_sub_f32_e32 v18, v18, v214
	v_sub_f32_e32 v19, v19, v214
	v_sub_f32_e32 v20, v20, v214
	v_sub_f32_e32 v21, v21, v214
	v_exp_f32_e32 v18, v18
	v_exp_f32_e32 v19, v19
	v_exp_f32_e32 v20, v20
	v_exp_f32_e32 v21, v21
	v_sub_f32_e32 v22, v22, v214
	v_sub_f32_e32 v23, v23, v214
	v_sub_f32_e32 v24, v24, v214
	v_sub_f32_e32 v25, v25, v214
	v_add_f32_e32 v216, v18, v19
	v_add_f32_e32 v217, v20, v21
	v_exp_f32_e32 v22, v22
	v_exp_f32_e32 v23, v23
	v_exp_f32_e32 v24, v24
	v_exp_f32_e32 v25, v25
	v_sub_f32_e32 v26, v26, v214
	v_sub_f32_e32 v27, v27, v214
	v_sub_f32_e32 v28, v28, v214
	v_sub_f32_e32 v29, v29, v214
	v_add_f32_e32 v216, v216, v22
	v_add_f32_e32 v217, v217, v23
	v_add_f32_e32 v216, v216, v24
	v_add_f32_e32 v217, v217, v25
	v_exp_f32_e32 v26, v26
	v_exp_f32_e32 v27, v27
	v_exp_f32_e32 v28, v28
	v_exp_f32_e32 v29, v29
	v_sub_f32_e32 v30, v30, v214
	v_sub_f32_e32 v31, v31, v214
	v_sub_f32_e32 v32, v32, v214
	v_sub_f32_e32 v33, v33, v214
	s_waitcnt lgkmcnt(0)
	v_mfma_f32_32x32x16_bf16 v[50:65], v[34:37], v[130:133], 0
	ds_read_b64_tr_b16 v[178:179], v219 offset:0
	ds_read_b64_tr_b16 v[180:181], v219 offset:512
	v_add_f32_e32 v216, v216, v26
	v_add_f32_e32 v217, v217, v27
	v_add_f32_e32 v216, v216, v28
	v_add_f32_e32 v217, v217, v29
	v_mfma_f32_32x32x16_bf16 v[34:49], v[38:41], v[130:133], 0
	ds_read_b64_tr_b16 v[170:171], v219 offset:1024
	ds_read_b64_tr_b16 v[172:173], v219 offset:1536
	v_exp_f32_e32 v30, v30
	v_exp_f32_e32 v31, v31
	v_exp_f32_e32 v32, v32
	v_exp_f32_e32 v33, v33
	v_mfma_f32_32x32x16_bf16 v[50:65], v[98:101], v[134:137], v[50:65]
	ds_read_b64_tr_b16 v[162:163], v219 offset:2048
	ds_read_b64_tr_b16 v[164:165], v219 offset:2560
	v_sub_f32_e32 v2, v2, v214
	v_sub_f32_e32 v3, v3, v214
	v_sub_f32_e32 v4, v4, v214
	v_sub_f32_e32 v5, v5, v214
	v_mfma_f32_32x32x16_bf16 v[34:49], v[102:105], v[134:137], v[34:49]
	ds_read_b64_tr_b16 v[158:159], v219 offset:3072
	ds_read_b64_tr_b16 v[160:161], v219 offset:3584
	v_add_f32_e32 v216, v216, v30
	v_add_f32_e32 v217, v217, v31
	v_add_f32_e32 v216, v216, v32
	v_add_f32_e32 v217, v217, v33
	v_mfma_f32_32x32x16_bf16 v[50:65], v[106:109], v[138:141], v[50:65]
	ds_read_b64_tr_b16 v[182:183], v219 offset:4096
	ds_read_b64_tr_b16 v[184:185], v219 offset:4608
	v_exp_f32_e32 v2, v2
	v_exp_f32_e32 v3, v3
	v_exp_f32_e32 v4, v4
	v_exp_f32_e32 v5, v5
	v_mfma_f32_32x32x16_bf16 v[34:49], v[110:113], v[138:141], v[34:49]
	ds_read_b64_tr_b16 v[174:175], v219 offset:5120
	ds_read_b64_tr_b16 v[176:177], v219 offset:5632
	v_sub_f32_e32 v6, v6, v214
	v_sub_f32_e32 v7, v7, v214
	v_sub_f32_e32 v8, v8, v214
	v_sub_f32_e32 v9, v9, v214
	v_mfma_f32_32x32x16_bf16 v[50:65], v[114:117], v[142:145], v[50:65]
	ds_read_b64_tr_b16 v[166:167], v219 offset:6144
	ds_read_b64_tr_b16 v[168:169], v219 offset:6656
	v_exp_f32_e32 v6, v6
	v_exp_f32_e32 v7, v7
	v_exp_f32_e32 v8, v8
	v_exp_f32_e32 v9, v9
	v_mfma_f32_32x32x16_bf16 v[34:49], v[118:121], v[142:145], v[34:49]
	ds_read_b64_tr_b16 v[154:155], v219 offset:7168
	ds_read_b64_tr_b16 v[156:157], v219 offset:7680
	v_sub_f32_e32 v10, v10, v214
	v_sub_f32_e32 v11, v11, v214
	v_sub_f32_e32 v12, v12, v214
	v_sub_f32_e32 v13, v13, v214
	v_mfma_f32_32x32x16_bf16 v[50:65], v[122:125], v[146:149], v[50:65]
	v_exp_f32_e32 v10, v10
	v_exp_f32_e32 v11, v11
	v_exp_f32_e32 v12, v12
	v_exp_f32_e32 v13, v13
	v_mfma_f32_32x32x16_bf16 v[34:49], v[126:129], v[146:149], v[34:49]
	v_sub_f32_e32 v14, v14, v214
	v_sub_f32_e32 v15, v15, v214
	v_sub_f32_e32 v16, v16, v214
	v_sub_f32_e32 v17, v17, v214
	v_mfma_f32_32x32x16_bf16 v[50:65], v[204:207], v[150:153], v[50:65]
	v_exp_f32_e32 v14, v14
	v_exp_f32_e32 v15, v15
	v_exp_f32_e32 v16, v16
	v_exp_f32_e32 v17, v17
	v_mfma_f32_32x32x16_bf16 v[34:49], v[208:211], v[150:153], v[34:49]
	s_cmp_lt_u32 s72, s77
	s_cbranch_scc1 .Lmla0_h0_nomask
; template <bool ALIBI>
; __device__ __forceinline__ void attn_sv(const LAS unsigned char* kb, int vfo, f32x16& p0, f32x16& p1, float& m, float& l, f32x16& o0, f32x16& o1, int hi, int tq, int kpos0, float slope2, bool causal) {
;     ...
;     if (causal) {
; #pragma unroll
;         for (int r = 0; r < 16; ++r) { const int kv = krel + (r & 3) + 8 * (r >> 2); if (kv > 0) p0[r] = -INFINITY; if (kv + 32 > 0) p1[r] = -INFINITY; } }
;     float rm = fmaxf(p0[0], p1[0]);
; #pragma unroll
;     for (int r = 1; r < 16; ++r) rm = fmaxf(rm, fmaxf(p0[r], p1[r]));
;     rm = xhalf_max(rm);
;     const float mn = fmaxf(m, rm), alpha = __builtin_amdgcn_exp2f(m - mn);
;     ...
;     const u32x4 pw0 = (u32x4){pg8::cvt_pk_bf16(p0[0], p0[1]), pg8::cvt_pk_bf16(p0[2], p0[3]), pg8::cvt_pk_bf16(p0[4], p0[5]), pg8::cvt_pk_bf16(p0[6], p0[7])};
;     const u32x4 pw1 = (u32x4){pg8::cvt_pk_bf16(p0[8], p0[9]), pg8::cvt_pk_bf16(p0[10], p0[11]), pg8::cvt_pk_bf16(p0[12], p0[13]), pg8::cvt_pk_bf16(p0[14], p0[15])};
;     const u32x4 pw2 = (u32x4){pg8::cvt_pk_bf16(p1[0], p1[1]), pg8::cvt_pk_bf16(p1[2], p1[3]), pg8::cvt_pk_bf16(p1[4], p1[5]), pg8::cvt_pk_bf16(p1[6], p1[7])};
;     const u32x4 pw3 = (u32x4){pg8::cvt_pk_bf16(p1[8], p1[9]), pg8::cvt_pk_bf16(p1[10], p1[11]), pg8::cvt_pk_bf16(p1[12], p1[13]), pg8::cvt_pk_bf16(p1[14], p1[15])};
;     asm volatile("s_waitcnt lgkmcnt(0)" ::: "memory"); __builtin_amdgcn_sched_barrier(0);
;     ...
;     o0 = __builtin_amdgcn_mfma_f32_32x32x16_bf16(ATT_VF(0), __builtin_bit_cast(bf16x8, pw0), o0, 0, 0, 0);
;     o1 = __builtin_amdgcn_mfma_f32_32x32x16_bf16(ATT_VF(4), __builtin_bit_cast(bf16x8, pw0), o1, 0, 0, 0);
;     o0 = __builtin_amdgcn_mfma_f32_32x32x16_bf16(ATT_VF(1), __builtin_bit_cast(bf16x8, pw1), o0, 0, 0, 0);
;     o1 = __builtin_amdgcn_mfma_f32_32x32x16_bf16(ATT_VF(5), __builtin_bit_cast(bf16x8, pw1), o1, 0, 0, 0);
;     o0 = __builtin_amdgcn_mfma_f32_32x32x16_bf16(ATT_VF(2), __builtin_bit_cast(bf16x8, pw2), o0, 0, 0, 0);
;     o1 = __builtin_amdgcn_mfma_f32_32x32x16_bf16(ATT_VF(6), __builtin_bit_cast(bf16x8, pw2), o1, 0, 0, 0);
;     o0 = __builtin_amdgcn_mfma_f32_32x32x16_bf16(ATT_VF(3), __builtin_bit_cast(bf16x8, pw3), o0, 0, 0, 0);
;     o1 = __builtin_amdgcn_mfma_f32_32x32x16_bf16(ATT_VF(7), __builtin_bit_cast(bf16x8, pw3), o1, 0, 0, 0);
	s_add_i32 s1, s72, 1
	s_nop 7
	s_nop 3
	v_lshl_add_u32 v220, s1, 6, v201
	v_sub_u32_e32 v220, 0, v220
	v_cmp_gt_i32_e64 s[8:9], 0, v220
	v_cmp_gt_i32_e64 s[10:11], 1, v220
	v_cmp_gt_i32_e64 s[12:13], 2, v220
	v_cmp_gt_i32_e64 s[14:15], 3, v220
	v_cmp_gt_i32_e64 s[16:17], 8, v220
	v_cmp_gt_i32_e64 s[18:19], 9, v220
	v_cmp_gt_i32_e64 s[20:21], 10, v220
	v_cmp_gt_i32_e64 s[22:23], 11, v220
	v_cndmask_b32_e64 v50, v50, v1, s[8:9]
	v_cndmask_b32_e64 v51, v51, v1, s[10:11]
	v_cndmask_b32_e64 v52, v52, v1, s[12:13]
	v_cndmask_b32_e64 v53, v53, v1, s[14:15]
	v_cndmask_b32_e64 v54, v54, v1, s[16:17]
	v_cndmask_b32_e64 v55, v55, v1, s[18:19]
	v_cndmask_b32_e64 v56, v56, v1, s[20:21]
	v_cndmask_b32_e64 v57, v57, v1, s[22:23]
	v_cmp_gt_i32_e64 s[8:9], 16, v220
	v_cmp_gt_i32_e64 s[10:11], 17, v220
	v_cmp_gt_i32_e64 s[12:13], 18, v220
	v_cmp_gt_i32_e64 s[14:15], 19, v220
	v_cmp_gt_i32_e64 s[16:17], 24, v220
	v_cmp_gt_i32_e64 s[18:19], 25, v220
	v_cmp_gt_i32_e64 s[20:21], 26, v220
	v_cmp_gt_i32_e64 s[22:23], 27, v220
	v_cndmask_b32_e64 v58, v58, v1, s[8:9]
	v_cndmask_b32_e64 v59, v59, v1, s[10:11]
	v_cndmask_b32_e64 v60, v60, v1, s[12:13]
	v_cndmask_b32_e64 v61, v61, v1, s[14:15]
	v_cndmask_b32_e64 v62, v62, v1, s[16:17]
	v_cndmask_b32_e64 v63, v63, v1, s[18:19]
	v_cndmask_b32_e64 v64, v64, v1, s[20:21]
	v_cndmask_b32_e64 v65, v65, v1, s[22:23]
	v_cmp_gt_i32_e64 s[8:9], 32, v220
	v_cmp_gt_i32_e64 s[10:11], 33, v220
	v_cmp_gt_i32_e64 s[12:13], 34, v220
	v_cmp_gt_i32_e64 s[14:15], 35, v220
	v_cmp_gt_i32_e64 s[16:17], 40, v220
	v_cmp_gt_i32_e64 s[18:19], 41, v220
	v_cmp_gt_i32_e64 s[20:21], 42, v220
	v_cmp_gt_i32_e64 s[22:23], 43, v220
	v_cndmask_b32_e64 v34, v34, v1, s[8:9]
	v_cndmask_b32_e64 v35, v35, v1, s[10:11]
	v_cndmask_b32_e64 v36, v36, v1, s[12:13]
	v_cndmask_b32_e64 v37, v37, v1, s[14:15]
	v_cndmask_b32_e64 v38, v38, v1, s[16:17]
	v_cndmask_b32_e64 v39, v39, v1, s[18:19]
	v_cndmask_b32_e64 v40, v40, v1, s[20:21]
	v_cndmask_b32_e64 v41, v41, v1, s[22:23]
	v_cmp_gt_i32_e64 s[8:9], 48, v220
	v_cmp_gt_i32_e64 s[10:11], 49, v220
	v_cmp_gt_i32_e64 s[12:13], 50, v220
	v_cmp_gt_i32_e64 s[14:15], 51, v220
	v_cmp_gt_i32_e64 s[16:17], 56, v220
	v_cmp_gt_i32_e64 s[18:19], 57, v220
	v_cmp_gt_i32_e64 s[20:21], 58, v220
	v_cmp_gt_i32_e64 s[22:23], 59, v220
	v_cndmask_b32_e64 v42, v42, v1, s[8:9]
	v_cndmask_b32_e64 v43, v43, v1, s[10:11]
	v_cndmask_b32_e64 v44, v44, v1, s[12:13]
	v_cndmask_b32_e64 v45, v45, v1, s[14:15]
	v_cndmask_b32_e64 v46, v46, v1, s[16:17]
	v_cndmask_b32_e64 v47, v47, v1, s[18:19]
	v_cndmask_b32_e64 v48, v48, v1, s[20:21]
	v_cndmask_b32_e64 v49, v49, v1, s[22:23]
.Lmla0_h0_nomask:
	s_nop 0
	v_cvt_pk_bf16_f32 v18, v18, v19
	v_cvt_pk_bf16_f32 v19, v20, v21
	v_cvt_pk_bf16_f32 v20, v22, v23
	v_cvt_pk_bf16_f32 v21, v24, v25
	v_add_f32_e32 v216, v216, v2
	v_add_f32_e32 v217, v217, v3
	s_waitcnt lgkmcnt(0)
	v_mfma_f32_32x32x16_bf16 v[66:81], v[178:181], v[18:21], v[66:81]
	v_add_f32_e32 v216, v216, v4
	v_add_f32_e32 v217, v217, v5
	v_cvt_pk_bf16_f32 v22, v26, v27
	v_cvt_pk_bf16_f32 v23, v28, v29
	v_cvt_pk_bf16_f32 v24, v30, v31
	v_cvt_pk_bf16_f32 v25, v32, v33
	v_mfma_f32_32x32x16_bf16 v[82:97], v[182:185], v[18:21], v[82:97]
	v_add_f32_e32 v216, v216, v6
	v_add_f32_e32 v217, v217, v7
	v_add_f32_e32 v216, v216, v8
	v_add_f32_e32 v217, v217, v9
	v_max3_f32 v218, v34, v35, v36
	v_max3_f32 v219, v50, v51, v52
	v_max3_f32 v218, v218, v37, v38
	v_max3_f32 v219, v219, v53, v54
	v_mfma_f32_32x32x16_bf16 v[66:81], v[170:173], v[22:25], v[66:81]
	v_cvt_pk_bf16_f32 v26, v2, v3
	v_cvt_pk_bf16_f32 v27, v4, v5
	v_cvt_pk_bf16_f32 v28, v6, v7
	v_cvt_pk_bf16_f32 v29, v8, v9
	v_max3_f32 v218, v218, v39, v40
	v_max3_f32 v219, v219, v55, v56
	v_max3_f32 v218, v218, v41, v42
	v_max3_f32 v219, v219, v57, v58
	v_mfma_f32_32x32x16_bf16 v[82:97], v[174:177], v[22:25], v[82:97]
	v_add_f32_e32 v216, v216, v10
	v_add_f32_e32 v217, v217, v11
	v_add_f32_e32 v216, v216, v12
	v_add_f32_e32 v217, v217, v13
	v_max3_f32 v218, v218, v43, v44
	v_max3_f32 v219, v219, v59, v60
	v_max3_f32 v218, v218, v45, v46
	v_max3_f32 v219, v219, v61, v62
	v_mfma_f32_32x32x16_bf16 v[66:81], v[162:165], v[26:29], v[66:81]
	v_add_f32_e32 v216, v216, v14
	v_add_f32_e32 v217, v217, v15
	v_add_f32_e32 v216, v216, v16
	v_add_f32_e32 v217, v217, v17
	v_max3_f32 v218, v218, v47, v48
	v_max3_f32 v219, v219, v63, v64
	v_max3_f32 v218, v218, v49, v219
	v_max_f32_e32 v218, v218, v65
	v_mfma_f32_32x32x16_bf16 v[82:97], v[166:169], v[26:29], v[82:97]
	v_cvt_pk_bf16_f32 v30, v10, v11
	v_cvt_pk_bf16_f32 v31, v12, v13
	v_cvt_pk_bf16_f32 v32, v14, v15
	v_cvt_pk_bf16_f32 v33, v16, v17
	v_mov_b32_e32 v219, v218
	v_add_f32_e32 v216, v216, v217
	v_fma_f32 v202, v202, v186, v216
	v_mfma_f32_32x32x16_bf16 v[66:81], v[158:161], v[30:33], v[66:81]
	v_permlane32_swap_b32_e32 v218, v219
	v_max3_f32 v203, v214, v218, v219
	v_sub_f32_e32 v218, v214, v203
	v_exp_f32_e32 v212, v218
	v_mfma_f32_32x32x16_bf16 v[82:97], v[154:157], v[30:33], v[82:97]
	s_cmp_eq_u32 s92, 0
	s_cbranch_scc1 .Lmla0_h0_full
	s_cmp_lg_u32 s88, 0
	s_cbranch_scc1 .Lmla0_h0_w2
	s_waitcnt vmcnt(3)
	s_branch .Lmla0_h0_bar

; #define LAS __attribute__((address_space(3)))
; template <int DQK>
; __device__ __forceinline__ void attn_qk(const LAS unsigned char* kb, int kfo, const bf16x8 (&qf)[DQK / 16], f32x16& p0, f32x16& p1) {
;     constexpr int ND0 = DQK / 16;
;     bf16x8 ka[ND0], kc[ND0];
; #pragma unroll
;     for (int d0 = 0; d0 < ND0; ++d0) { ka[d0] = *(const LAS bf16x8*)(kb + kfo + d0 * 2048); kc[d0] = *(const LAS bf16x8*)(kb + kfo + d0 * 2048 + 512); }
;     __builtin_amdgcn_sched_barrier(0);
; #pragma unroll
;     for (int r = 0; r < 16; ++r) { p0[r] = 0.f; p1[r] = 0.f; }
; #pragma unroll
;     for (int d0 = 0; d0 < ND0; ++d0) {
;         p0 = __builtin_amdgcn_mfma_f32_32x32x16_bf16(ka[d0], qf[d0], p0, 0, 0, 0);
;         p1 = __builtin_amdgcn_mfma_f32_32x32x16_bf16(kc[d0], qf[d0], p1, 0, 0, 0);
;     }
; template <bool ALIBI>
; __device__ __forceinline__ void attn_sv(const LAS unsigned char* kb, int vfo, f32x16& p0, f32x16& p1, float& m, float& l, f32x16& o0, f32x16& o1, int hi, int tq, int kpos0, float slope2, bool causal) {
;     ...
;     float ls = 0.f;
; #pragma unroll
;     for (int r = 0; r < 16; ++r) { p0[r] = __builtin_amdgcn_exp2f(p0[r] - mn); p1[r] = __builtin_amdgcn_exp2f(p1[r] - mn); ls += p0[r] + p1[r]; }
;     l = l * alpha + ls;
; #pragma unroll
;     for (int r = 0; r < 16; ++r) { o0[r] *= alpha; o1[r] *= alpha; }
.Lmla0_h1_noiss:
	v_cmp_neq_f32_e32 vcc, 1.0, v212
	s_cbranch_vccz .Lmla0_h1_noresc
	v_pk_mul_f32 v[66:67], v[66:67], v[212:213] op_sel_hi:[1,0]
	v_pk_mul_f32 v[68:69], v[68:69], v[212:213] op_sel_hi:[1,0]
	v_pk_mul_f32 v[70:71], v[70:71], v[212:213] op_sel_hi:[1,0]
	v_pk_mul_f32 v[72:73], v[72:73], v[212:213] op_sel_hi:[1,0]
	v_pk_mul_f32 v[74:75], v[74:75], v[212:213] op_sel_hi:[1,0]
	v_pk_mul_f32 v[76:77], v[76:77], v[212:213] op_sel_hi:[1,0]
	v_pk_mul_f32 v[78:79], v[78:79], v[212:213] op_sel_hi:[1,0]
	v_pk_mul_f32 v[80:81], v[80:81], v[212:213] op_sel_hi:[1,0]
	v_pk_mul_f32 v[82:83], v[82:83], v[212:213] op_sel_hi:[1,0]
	v_pk_mul_f32 v[84:85], v[84:85], v[212:213] op_sel_hi:[1,0]
	v_pk_mul_f32 v[86:87], v[86:87], v[212:213] op_sel_hi:[1,0]
	v_pk_mul_f32 v[88:89], v[88:89], v[212:213] op_sel_hi:[1,0]
	v_pk_mul_f32 v[90:91], v[90:91], v[212:213] op_sel_hi:[1,0]
	v_pk_mul_f32 v[92:93], v[92:93], v[212:213] op_sel_hi:[1,0]
	v_pk_mul_f32 v[94:95], v[94:95], v[212:213] op_sel_hi:[1,0]
	v_pk_mul_f32 v[96:97], v[96:97], v[212:213] op_sel_hi:[1,0]
.Lmla0_h1_noresc:
	v_sub_f32_e32 v50, v50, v203
	v_sub_f32_e32 v51, v51, v203
	v_sub_f32_e32 v52, v52, v203
	v_sub_f32_e32 v53, v53, v203
	v_exp_f32_e32 v50, v50
	v_exp_f32_e32 v51, v51
	v_exp_f32_e32 v52, v52
	v_exp_f32_e32 v53, v53
	v_sub_f32_e32 v54, v54, v203
	v_sub_f32_e32 v55, v55, v203
	v_sub_f32_e32 v56, v56, v203
	v_sub_f32_e32 v57, v57, v203
	v_add_f32_e32 v216, v50, v51
	v_add_f32_e32 v217, v52, v53
	v_exp_f32_e32 v54, v54
	v_exp_f32_e32 v55, v55
	v_exp_f32_e32 v56, v56
	v_exp_f32_e32 v57, v57
	v_sub_f32_e32 v58, v58, v203
	v_sub_f32_e32 v59, v59, v203
	v_sub_f32_e32 v60, v60, v203
	v_sub_f32_e32 v61, v61, v203
	v_add_f32_e32 v216, v216, v54
	v_add_f32_e32 v217, v217, v55
	v_add_f32_e32 v216, v216, v56
	v_add_f32_e32 v217, v217, v57
	v_exp_f32_e32 v58, v58
	v_exp_f32_e32 v59, v59
	v_exp_f32_e32 v60, v60
	v_exp_f32_e32 v61, v61
	v_sub_f32_e32 v62, v62, v203
	v_sub_f32_e32 v63, v63, v203
	v_sub_f32_e32 v64, v64, v203
	v_sub_f32_e32 v65, v65, v203
	s_cmp_eq_u32 s93, 0
	s_cbranch_scc1 .Lmla0_h1_noqk
	s_waitcnt lgkmcnt(0)
	v_mfma_f32_32x32x16_bf16 v[18:33], v[2:5], v[130:133], 0
	ds_read_b64_tr_b16 v[178:179], v219 offset:0
	ds_read_b64_tr_b16 v[180:181], v219 offset:512
	v_add_f32_e32 v216, v216, v58
	v_add_f32_e32 v217, v217, v59
	v_add_f32_e32 v216, v216, v60
	v_add_f32_e32 v217, v217, v61
	v_mfma_f32_32x32x16_bf16 v[2:17], v[6:9], v[130:133], 0
	ds_read_b64_tr_b16 v[170:171], v219 offset:1024
	ds_read_b64_tr_b16 v[172:173], v219 offset:1536
	v_exp_f32_e32 v62, v62
	v_exp_f32_e32 v63, v63
	v_exp_f32_e32 v64, v64
	v_exp_f32_e32 v65, v65
	v_mfma_f32_32x32x16_bf16 v[18:33], v[98:101], v[134:137], v[18:33]
	ds_read_b64_tr_b16 v[162:163], v219 offset:2048
	ds_read_b64_tr_b16 v[164:165], v219 offset:2560
	v_sub_f32_e32 v34, v34, v203
	v_sub_f32_e32 v35, v35, v203
	v_sub_f32_e32 v36, v36, v203
	v_sub_f32_e32 v37, v37, v203
	v_mfma_f32_32x32x16_bf16 v[2:17], v[102:105], v[134:137], v[2:17]
	ds_read_b64_tr_b16 v[158:159], v219 offset:3072
	ds_read_b64_tr_b16 v[160:161], v219 offset:3584
	v_add_f32_e32 v216, v216, v62
	v_add_f32_e32 v217, v217, v63
	v_add_f32_e32 v216, v216, v64
	v_add_f32_e32 v217, v217, v65
	v_mfma_f32_32x32x16_bf16 v[18:33], v[106:109], v[138:141], v[18:33]
	ds_read_b64_tr_b16 v[182:183], v219 offset:4096
	ds_read_b64_tr_b16 v[184:185], v219 offset:4608
	v_exp_f32_e32 v34, v34
	v_exp_f32_e32 v35, v35
	v_exp_f32_e32 v36, v36
	v_exp_f32_e32 v37, v37
	v_mfma_f32_32x32x16_bf16 v[2:17], v[110:113], v[138:141], v[2:17]
	ds_read_b64_tr_b16 v[174:175], v219 offset:5120
	ds_read_b64_tr_b16 v[176:177], v219 offset:5632
	v_sub_f32_e32 v38, v38, v203
	v_sub_f32_e32 v39, v39, v203
	v_sub_f32_e32 v40, v40, v203
	v_sub_f32_e32 v41, v41, v203
	v_mfma_f32_32x32x16_bf16 v[18:33], v[114:117], v[142:145], v[18:33]
	ds_read_b64_tr_b16 v[166:167], v219 offset:6144
	ds_read_b64_tr_b16 v[168:169], v219 offset:6656
	v_exp_f32_e32 v38, v38
	v_exp_f32_e32 v39, v39
	v_exp_f32_e32 v40, v40
	v_exp_f32_e32 v41, v41
	v_mfma_f32_32x32x16_bf16 v[2:17], v[118:121], v[142:145], v[2:17]
	ds_read_b64_tr_b16 v[154:155], v219 offset:7168
	ds_read_b64_tr_b16 v[156:157], v219 offset:7680
	v_sub_f32_e32 v42, v42, v203
	v_sub_f32_e32 v43, v43, v203
	v_sub_f32_e32 v44, v44, v203
	v_sub_f32_e32 v45, v45, v203
	v_mfma_f32_32x32x16_bf16 v[18:33], v[122:125], v[146:149], v[18:33]
	v_exp_f32_e32 v42, v42
	v_exp_f32_e32 v43, v43
	v_exp_f32_e32 v44, v44
	v_exp_f32_e32 v45, v45
	v_mfma_f32_32x32x16_bf16 v[2:17], v[126:129], v[146:149], v[2:17]
	v_sub_f32_e32 v46, v46, v203
	v_sub_f32_e32 v47, v47, v203
	v_sub_f32_e32 v48, v48, v203
	v_sub_f32_e32 v49, v49, v203
	v_mfma_f32_32x32x16_bf16 v[18:33], v[204:207], v[150:153], v[18:33]
	v_exp_f32_e32 v46, v46
	v_exp_f32_e32 v47, v47
	v_exp_f32_e32 v48, v48
	v_exp_f32_e32 v49, v49
	v_mfma_f32_32x32x16_bf16 v[2:17], v[208:211], v[150:153], v[2:17]
	s_add_i32 s1, s72, 2
	s_cmp_lt_u32 s1, s77
	s_cbranch_scc1 .Lmla0_h1_nomask
; template <bool ALIBI>
; __device__ __forceinline__ void attn_sv(const LAS unsigned char* kb, int vfo, f32x16& p0, f32x16& p1, float& m, float& l, f32x16& o0, f32x16& o1, int hi, int tq, int kpos0, float slope2, bool causal) {
;     ...
;     if (causal) {
; #pragma unroll
;         for (int r = 0; r < 16; ++r) { const int kv = krel + (r & 3) + 8 * (r >> 2); if (kv > 0) p0[r] = -INFINITY; if (kv + 32 > 0) p1[r] = -INFINITY; } }
	s_nop 7
	s_nop 3
	v_lshl_add_u32 v220, s1, 6, v201
	v_sub_u32_e32 v220, 0, v220
	v_cmp_gt_i32_e64 s[8:9], 0, v220
	v_cmp_gt_i32_e64 s[10:11], 1, v220
	v_cmp_gt_i32_e64 s[12:13], 2, v220
	v_cmp_gt_i32_e64 s[14:15], 3, v220
	v_cmp_gt_i32_e64 s[16:17], 8, v220
	v_cmp_gt_i32_e64 s[18:19], 9, v220
	v_cmp_gt_i32_e64 s[20:21], 10, v220
	v_cmp_gt_i32_e64 s[22:23], 11, v220
	v_cndmask_b32_e64 v18, v18, v1, s[8:9]
	v_cndmask_b32_e64 v19, v19, v1, s[10:11]
	v_cndmask_b32_e64 v20, v20, v1, s[12:13]
	v_cndmask_b32_e64 v21, v21, v1, s[14:15]
	v_cndmask_b32_e64 v22, v22, v1, s[16:17]
	v_cndmask_b32_e64 v23, v23, v1, s[18:19]
	v_cndmask_b32_e64 v24, v24, v1, s[20:21]
	v_cndmask_b32_e64 v25, v25, v1, s[22:23]
	v_cmp_gt_i32_e64 s[8:9], 16, v220
	v_cmp_gt_i32_e64 s[10:11], 17, v220
	v_cmp_gt_i32_e64 s[12:13], 18, v220
	v_cmp_gt_i32_e64 s[14:15], 19, v220
	v_cmp_gt_i32_e64 s[16:17], 24, v220
	v_cmp_gt_i32_e64 s[18:19], 25, v220
	v_cmp_gt_i32_e64 s[20:21], 26, v220
	v_cmp_gt_i32_e64 s[22:23], 27, v220
	v_cndmask_b32_e64 v26, v26, v1, s[8:9]
	v_cndmask_b32_e64 v27, v27, v1, s[10:11]
	v_cndmask_b32_e64 v28, v28, v1, s[12:13]
	v_cndmask_b32_e64 v29, v29, v1, s[14:15]
	v_cndmask_b32_e64 v30, v30, v1, s[16:17]
	v_cndmask_b32_e64 v31, v31, v1, s[18:19]
	v_cndmask_b32_e64 v32, v32, v1, s[20:21]
	v_cndmask_b32_e64 v33, v33, v1, s[22:23]
	v_cmp_gt_i32_e64 s[8:9], 32, v220
	v_cmp_gt_i32_e64 s[10:11], 33, v220
	v_cmp_gt_i32_e64 s[12:13], 34, v220
	v_cmp_gt_i32_e64 s[14:15], 35, v220
	v_cmp_gt_i32_e64 s[16:17], 40, v220
	v_cmp_gt_i32_e64 s[18:19], 41, v220
	v_cmp_gt_i32_e64 s[20:21], 42, v220
	v_cmp_gt_i32_e64 s[22:23], 43, v220
	v_cndmask_b32_e64 v2, v2, v1, s[8:9]
	v_cndmask_b32_e64 v3, v3, v1, s[10:11]
	v_cndmask_b32_e64 v4, v4, v1, s[12:13]
	v_cndmask_b32_e64 v5, v5, v1, s[14:15]
	v_cndmask_b32_e64 v6, v6, v1, s[16:17]
	v_cndmask_b32_e64 v7, v7, v1, s[18:19]
	v_cndmask_b32_e64 v8, v8, v1, s[20:21]
	v_cndmask_b32_e64 v9, v9, v1, s[22:23]
	v_cmp_gt_i32_e64 s[8:9], 48, v220
	v_cmp_gt_i32_e64 s[10:11], 49, v220
	v_cmp_gt_i32_e64 s[12:13], 50, v220
	v_cmp_gt_i32_e64 s[14:15], 51, v220
	v_cmp_gt_i32_e64 s[16:17], 56, v220
	v_cmp_gt_i32_e64 s[18:19], 57, v220
	v_cmp_gt_i32_e64 s[20:21], 58, v220
	v_cmp_gt_i32_e64 s[22:23], 59, v220
	v_cndmask_b32_e64 v10, v10, v1, s[8:9]
	v_cndmask_b32_e64 v11, v11, v1, s[10:11]
	v_cndmask_b32_e64 v12, v12, v1, s[12:13]
	v_cndmask_b32_e64 v13, v13, v1, s[14:15]
	v_cndmask_b32_e64 v14, v14, v1, s[16:17]
	v_cndmask_b32_e64 v15, v15, v1, s[18:19]
	v_cndmask_b32_e64 v16, v16, v1, s[20:21]
	v_cndmask_b32_e64 v17, v17, v1, s[22:23]
.Lmla0_h1_nomask:
	s_branch .Lmla0_h1_qkdone
; __device__ __forceinline__ unsigned cvt_pk_bf16(float lo, float hi) { const f32x2_t_ v = {lo, hi}; const bf16x2_t_ b = __builtin_convertvector(v, bf16x2_t_); return __builtin_bit_cast(unsigned, b); }
; template <bool ALIBI>
; __device__ __forceinline__ void attn_sv(const LAS unsigned char* kb, int vfo, f32x16& p0, f32x16& p1, float& m, float& l, f32x16& o0, f32x16& o1, int hi, int tq, int kpos0, float slope2, bool causal) {
;     ...
;     float rm = fmaxf(p0[0], p1[0]);
; #pragma unroll
;     for (int r = 1; r < 16; ++r) rm = fmaxf(rm, fmaxf(p0[r], p1[r]));
;     rm = xhalf_max(rm);
;     const float mn = fmaxf(m, rm), alpha = __builtin_amdgcn_exp2f(m - mn);
;     ...
;     const u32x4 pw0 = (u32x4){pg8::cvt_pk_bf16(p0[0], p0[1]), pg8::cvt_pk_bf16(p0[2], p0[3]), pg8::cvt_pk_bf16(p0[4], p0[5]), pg8::cvt_pk_bf16(p0[6], p0[7])};
;     const u32x4 pw1 = (u32x4){pg8::cvt_pk_bf16(p0[8], p0[9]), pg8::cvt_pk_bf16(p0[10], p0[11]), pg8::cvt_pk_bf16(p0[12], p0[13]), pg8::cvt_pk_bf16(p0[14], p0[15])};
;     const u32x4 pw2 = (u32x4){pg8::cvt_pk_bf16(p1[0], p1[1]), pg8::cvt_pk_bf16(p1[2], p1[3]), pg8::cvt_pk_bf16(p1[4], p1[5]), pg8::cvt_pk_bf16(p1[6], p1[7])};
;     const u32x4 pw3 = (u32x4){pg8::cvt_pk_bf16(p1[8], p1[9]), pg8::cvt_pk_bf16(p1[10], p1[11]), pg8::cvt_pk_bf16(p1[12], p1[13]), pg8::cvt_pk_bf16(p1[14], p1[15])};
;     asm volatile("s_waitcnt lgkmcnt(0)" ::: "memory"); __builtin_amdgcn_sched_barrier(0);
;     ...
;     o0 = __builtin_amdgcn_mfma_f32_32x32x16_bf16(ATT_VF(0), __builtin_bit_cast(bf16x8, pw0), o0, 0, 0, 0);
;     o1 = __builtin_amdgcn_mfma_f32_32x32x16_bf16(ATT_VF(4), __builtin_bit_cast(bf16x8, pw0), o1, 0, 0, 0);
;     o0 = __builtin_amdgcn_mfma_f32_32x32x16_bf16(ATT_VF(1), __builtin_bit_cast(bf16x8, pw1), o0, 0, 0, 0);
;     o1 = __builtin_amdgcn_mfma_f32_32x32x16_bf16(ATT_VF(5), __builtin_bit_cast(bf16x8, pw1), o1, 0, 0, 0);
;     o0 = __builtin_amdgcn_mfma_f32_32x32x16_bf16(ATT_VF(2), __builtin_bit_cast(bf16x8, pw2), o0, 0, 0, 0);
;     o1 = __builtin_amdgcn_mfma_f32_32x32x16_bf16(ATT_VF(6), __builtin_bit_cast(bf16x8, pw2), o1, 0, 0, 0);
;     o0 = __builtin_amdgcn_mfma_f32_32x32x16_bf16(ATT_VF(3), __builtin_bit_cast(bf16x8, pw3), o0, 0, 0, 0);
;     o1 = __builtin_amdgcn_mfma_f32_32x32x16_bf16(ATT_VF(7), __builtin_bit_cast(bf16x8, pw3), o1, 0, 0, 0);
.Lmla0_h1_noqk:
	ds_read_b64_tr_b16 v[178:179], v219 offset:0
	ds_read_b64_tr_b16 v[180:181], v219 offset:512
	ds_read_b64_tr_b16 v[170:171], v219 offset:1024
	ds_read_b64_tr_b16 v[172:173], v219 offset:1536
	ds_read_b64_tr_b16 v[162:163], v219 offset:2048
	ds_read_b64_tr_b16 v[164:165], v219 offset:2560
	ds_read_b64_tr_b16 v[158:159], v219 offset:3072
	ds_read_b64_tr_b16 v[160:161], v219 offset:3584
	ds_read_b64_tr_b16 v[182:183], v219 offset:4096
	ds_read_b64_tr_b16 v[184:185], v219 offset:4608
	ds_read_b64_tr_b16 v[174:175], v219 offset:5120
	ds_read_b64_tr_b16 v[176:177], v219 offset:5632
	ds_read_b64_tr_b16 v[166:167], v219 offset:6144
	ds_read_b64_tr_b16 v[168:169], v219 offset:6656
	ds_read_b64_tr_b16 v[154:155], v219 offset:7168
	ds_read_b64_tr_b16 v[156:157], v219 offset:7680
	v_add_f32_e32 v216, v216, v58
	v_add_f32_e32 v217, v217, v59
	v_add_f32_e32 v216, v216, v60
	v_add_f32_e32 v217, v217, v61
	v_exp_f32_e32 v62, v62
	v_exp_f32_e32 v63, v63
	v_exp_f32_e32 v64, v64
	v_exp_f32_e32 v65, v65
	v_sub_f32_e32 v34, v34, v203
	v_sub_f32_e32 v35, v35, v203
	v_sub_f32_e32 v36, v36, v203
	v_sub_f32_e32 v37, v37, v203
	v_add_f32_e32 v216, v216, v62
	v_add_f32_e32 v217, v217, v63
	v_add_f32_e32 v216, v216, v64
	v_add_f32_e32 v217, v217, v65
	v_exp_f32_e32 v34, v34
	v_exp_f32_e32 v35, v35
	v_exp_f32_e32 v36, v36
	v_exp_f32_e32 v37, v37
	v_sub_f32_e32 v38, v38, v203
	v_sub_f32_e32 v39, v39, v203
	v_sub_f32_e32 v40, v40, v203
	v_sub_f32_e32 v41, v41, v203
	v_exp_f32_e32 v38, v38
	v_exp_f32_e32 v39, v39
	v_exp_f32_e32 v40, v40
	v_exp_f32_e32 v41, v41
	v_sub_f32_e32 v42, v42, v203
	v_sub_f32_e32 v43, v43, v203
	v_sub_f32_e32 v44, v44, v203
	v_sub_f32_e32 v45, v45, v203
	v_exp_f32_e32 v42, v42
	v_exp_f32_e32 v43, v43
	v_exp_f32_e32 v44, v44
	v_exp_f32_e32 v45, v45
	v_sub_f32_e32 v46, v46, v203
	v_sub_f32_e32 v47, v47, v203
	v_sub_f32_e32 v48, v48, v203
	v_sub_f32_e32 v49, v49, v203
	v_exp_f32_e32 v46, v46
	v_exp_f32_e32 v47, v47
	v_exp_f32_e32 v48, v48
	v_exp_f32_e32 v49, v49
.Lmla0_h1_qkdone:
	s_nop 0
	v_cvt_pk_bf16_f32 v50, v50, v51
	v_cvt_pk_bf16_f32 v51, v52, v53
	v_cvt_pk_bf16_f32 v52, v54, v55
	v_cvt_pk_bf16_f32 v53, v56, v57
	v_add_f32_e32 v216, v216, v34
	v_add_f32_e32 v217, v217, v35
	s_waitcnt lgkmcnt(0)
	v_mfma_f32_32x32x16_bf16 v[66:81], v[178:181], v[50:53], v[66:81]
	v_add_f32_e32 v216, v216, v36
	v_add_f32_e32 v217, v217, v37
	v_cvt_pk_bf16_f32 v54, v58, v59
	v_cvt_pk_bf16_f32 v55, v60, v61
	v_cvt_pk_bf16_f32 v56, v62, v63
	v_cvt_pk_bf16_f32 v57, v64, v65
	v_mfma_f32_32x32x16_bf16 v[82:97], v[182:185], v[50:53], v[82:97]
	v_add_f32_e32 v216, v216, v38
	v_add_f32_e32 v217, v217, v39
	v_add_f32_e32 v216, v216, v40
	v_add_f32_e32 v217, v217, v41
	v_max3_f32 v218, v2, v3, v4
	v_max3_f32 v219, v18, v19, v20
	v_max3_f32 v218, v218, v5, v6
	v_max3_f32 v219, v219, v21, v22
	v_mfma_f32_32x32x16_bf16 v[66:81], v[170:173], v[54:57], v[66:81]
	v_cvt_pk_bf16_f32 v58, v34, v35
	v_cvt_pk_bf16_f32 v59, v36, v37
	v_cvt_pk_bf16_f32 v60, v38, v39
	v_cvt_pk_bf16_f32 v61, v40, v41
	v_max3_f32 v218, v218, v7, v8
	v_max3_f32 v219, v219, v23, v24
	v_max3_f32 v218, v218, v9, v10
	v_max3_f32 v219, v219, v25, v26
	v_mfma_f32_32x32x16_bf16 v[82:97], v[174:177], v[54:57], v[82:97]
	v_add_f32_e32 v216, v216, v42
	v_add_f32_e32 v217, v217, v43
	v_add_f32_e32 v216, v216, v44
	v_add_f32_e32 v217, v217, v45
	v_max3_f32 v218, v218, v11, v12
	v_max3_f32 v219, v219, v27, v28
	v_max3_f32 v218, v218, v13, v14
	v_max3_f32 v219, v219, v29, v30
	v_mfma_f32_32x32x16_bf16 v[66:81], v[162:165], v[58:61], v[66:81]
	v_add_f32_e32 v216, v216, v46
	v_add_f32_e32 v217, v217, v47
	v_add_f32_e32 v216, v216, v48
	v_add_f32_e32 v217, v217, v49
	v_max3_f32 v218, v218, v15, v16
	v_max3_f32 v219, v219, v31, v32
	v_max3_f32 v218, v218, v17, v219
	v_max_f32_e32 v218, v218, v33
	v_mfma_f32_32x32x16_bf16 v[82:97], v[166:169], v[58:61], v[82:97]
	v_cvt_pk_bf16_f32 v62, v42, v43
	v_cvt_pk_bf16_f32 v63, v44, v45
	v_cvt_pk_bf16_f32 v64, v46, v47
	v_cvt_pk_bf16_f32 v65, v48, v49
	v_mov_b32_e32 v219, v218
	v_add_f32_e32 v216, v216, v217
	v_fma_f32 v202, v202, v212, v216
	v_mfma_f32_32x32x16_bf16 v[66:81], v[158:161], v[62:65], v[66:81]
	v_permlane32_swap_b32_e32 v218, v219
	v_max3_f32 v214, v203, v218, v219
	v_sub_f32_e32 v218, v203, v214
	v_exp_f32_e32 v186, v218
	v_mfma_f32_32x32x16_bf16 v[82:97], v[154:157], v[62:65], v[82:97]
	s_cmp_eq_u32 s92, 0
	s_cbranch_scc1 .Lmla0_h1_full
	s_cmp_lg_u32 s88, 0
	s_cbranch_scc1 .Lmla0_h1_w2
	s_waitcnt vmcnt(3)
	s_branch .Lmla0_h1_bar

; __device__ __forceinline__ void route_one(const f32x4 lg, const f32x4 rb, int lane, int& mye, float& myw) {
;     const float s0 = __builtin_amdgcn_rcpf(1.f + __expf(-lg[0])), s1 = __builtin_amdgcn_rcpf(1.f + __expf(-lg[1])), s2 = __builtin_amdgcn_rcpf(1.f + __expf(-lg[2])), s3 = __builtin_amdgcn_rcpf(1.f + __expf(-lg[3]));
;     float c0 = s0 + rb[0], c1 = s1 + rb[1], c2 = s2 + rb[2], c3 = s3 + rb[3];
;     float a = fmaxf(c0, c1), bq = fminf(c0, c1);
;     { const float hi2 = fmaxf(c2, c3), lo2 = fminf(c2, c3); const float na = fmaxf(a, hi2), nb = fmaxf(fminf(a, hi2), fmaxf(bq, lo2)); a = na; bq = nb; }
; #pragma unroll
;     for (int o = 1; o < 8; o <<= 1) { const float oa = __shfl_xor(a, o), ob = __shfl_xor(bq, o); const float na = fmaxf(a, oa), nb = fmaxf(fminf(a, oa), fmaxf(bq, ob)); a = na; bq = nb; }
;     const float gs = a + bq; const int grp = lane >> 3;
;     int rank = 0;
; #pragma unroll
;     for (int j = 0; j < 8; ++j) { const float og = __shfl(gs, j * 8); rank += (og > gs || (og == gs && j < grp)) ? 1 : 0; }
.LBB0_1483:
	v_lshlrev_b32_e32 v74, 2, v1
	v_lshl_or_b32 v75, v1, 2, 1
	v_lshl_or_b32 v76, v1, 2, 2
	v_lshl_or_b32 v77, v1, 2, 3
	v_mul_f32_e32 v18, 0xbfb8aa3b, v18
	v_mul_f32_e32 v14, 0xbfb8aa3b, v14
	v_mul_f32_e32 v19, 0xbfb8aa3b, v19
	v_mul_f32_e32 v15, 0xbfb8aa3b, v15
	v_mul_f32_e32 v20, 0xbfb8aa3b, v20
	v_mul_f32_e32 v16, 0xbfb8aa3b, v16
	v_mul_f32_e32 v21, 0xbfb8aa3b, v21
	v_mul_f32_e32 v17, 0xbfb8aa3b, v17
	v_exp_f32_e32 v18, v18
	v_exp_f32_e32 v14, v14
	v_exp_f32_e32 v19, v19
	v_exp_f32_e32 v15, v15
	v_exp_f32_e32 v20, v20
	v_exp_f32_e32 v16, v16
	v_exp_f32_e32 v21, v21
	v_exp_f32_e32 v17, v17
	v_add_f32_e32 v18, 1.0, v18
	v_add_f32_e32 v14, 1.0, v14
	v_add_f32_e32 v19, 1.0, v19
	v_add_f32_e32 v15, 1.0, v15
	v_add_f32_e32 v20, 1.0, v20
	v_add_f32_e32 v16, 1.0, v16
	v_add_f32_e32 v21, 1.0, v21
	v_add_f32_e32 v17, 1.0, v17
	v_rcp_f32_e32 v18, v18
	v_rcp_f32_e32 v14, v14
	v_rcp_f32_e32 v19, v19
	v_rcp_f32_e32 v15, v15
	v_rcp_f32_e32 v20, v20
	v_rcp_f32_e32 v16, v16
	v_rcp_f32_e32 v21, v21
	v_rcp_f32_e32 v17, v17
	v_add_f32_e32 v33, v2, v18
	v_add_f32_e32 v61, v2, v14
	v_add_f32_e32 v34, v3, v19
	v_add_f32_e32 v62, v3, v15
	v_add_f32_e32 v35, v4, v20
	v_add_f32_e32 v63, v4, v16
	v_add_f32_e32 v36, v5, v21
	v_add_f32_e32 v64, v5, v17
	v_max_f32_e32 v37, v33, v34
	v_max_f32_e32 v65, v61, v62
	v_min_f32_e32 v38, v33, v34
	v_min_f32_e32 v66, v61, v62
	v_max_f32_e32 v39, v35, v36
	v_max_f32_e32 v67, v63, v64
	v_min_f32_e32 v40, v35, v36
	v_min_f32_e32 v68, v63, v64
	v_min_f32_e32 v59, v37, v39
	v_min_f32_e32 v72, v65, v67
	v_max_f32_e32 v37, v37, v39
	v_max_f32_e32 v65, v65, v67
	v_max3_f32 v38, v59, v38, v40
	v_max3_f32 v66, v72, v66, v68
	v_min_f32_dpp v40, v37, v37 quad_perm:[1,0,3,2] row_mask:0xf bank_mask:0xf
	v_min_f32_dpp v68, v65, v65 quad_perm:[1,0,3,2] row_mask:0xf bank_mask:0xf
	v_max_f32_dpp v38, v38, v38 quad_perm:[1,0,3,2] row_mask:0xf bank_mask:0xf
	v_max_f32_dpp v66, v66, v66 quad_perm:[1,0,3,2] row_mask:0xf bank_mask:0xf
	v_max_f32_dpp v37, v37, v37 quad_perm:[1,0,3,2] row_mask:0xf bank_mask:0xf
	v_max_f32_dpp v65, v65, v65 quad_perm:[1,0,3,2] row_mask:0xf bank_mask:0xf
	v_max_f32_e32 v38, v38, v40
	v_max_f32_e32 v66, v66, v68
	v_min_f32_dpp v40, v37, v37 quad_perm:[2,3,0,1] row_mask:0xf bank_mask:0xf
	v_min_f32_dpp v68, v65, v65 quad_perm:[2,3,0,1] row_mask:0xf bank_mask:0xf
	v_max_f32_dpp v38, v38, v38 quad_perm:[2,3,0,1] row_mask:0xf bank_mask:0xf
	v_max_f32_dpp v66, v66, v66 quad_perm:[2,3,0,1] row_mask:0xf bank_mask:0xf
	v_max_f32_dpp v37, v37, v37 quad_perm:[2,3,0,1] row_mask:0xf bank_mask:0xf
	v_max_f32_dpp v65, v65, v65 quad_perm:[2,3,0,1] row_mask:0xf bank_mask:0xf
	v_max_f32_e32 v38, v38, v40
	v_max_f32_e32 v66, v66, v68
	v_min_f32_dpp v40, v37, v37 row_half_mirror row_mask:0xf bank_mask:0xf
	v_min_f32_dpp v68, v65, v65 row_half_mirror row_mask:0xf bank_mask:0xf
	v_max_f32_dpp v38, v38, v38 row_half_mirror row_mask:0xf bank_mask:0xf
	v_max_f32_dpp v66, v66, v66 row_half_mirror row_mask:0xf bank_mask:0xf
	v_max_f32_dpp v37, v37, v37 row_half_mirror row_mask:0xf bank_mask:0xf
	v_max_f32_dpp v65, v65, v65 row_half_mirror row_mask:0xf bank_mask:0xf
	v_max_f32_e32 v38, v38, v40
	v_max_f32_e32 v66, v66, v68
	v_add_f32_e32 v59, v37, v38
	v_add_f32_e32 v72, v65, v66
	v_mov_b32_e32 v60, 0
	v_mov_b32_e32 v73, 0
	v_readlane_b32 s48, v59, 0
	v_readlane_b32 s52, v72, 0
	s_nop 1
	v_cmp_gt_f32_e32 vcc, s48, v59
	v_cmp_gt_f32_e64 s[50:51], s52, v72
	v_cmp_eq_f32_e64 s[46:47], s48, v59
	v_cmp_eq_f32_e64 s[40:41], s52, v72
	v_addc_co_u32_e32 v60, vcc, 0, v60, vcc
	v_addc_co_u32_e64 v73, s[50:51], 0, v73, s[50:51]
	s_and_b64 s[46:47], s[46:47], s[4:5]
	s_and_b64 s[40:41], s[40:41], s[4:5]
	s_nop 0
	v_addc_co_u32_e64 v60, s[46:47], 0, v60, s[46:47]
	v_addc_co_u32_e64 v73, s[40:41], 0, v73, s[40:41]
	v_readlane_b32 s48, v59, 8
	v_readlane_b32 s52, v72, 8
	s_nop 1
	v_cmp_gt_f32_e32 vcc, s48, v59
	v_cmp_gt_f32_e64 s[50:51], s52, v72
	v_cmp_eq_f32_e64 s[46:47], s48, v59
	v_cmp_eq_f32_e64 s[40:41], s52, v72
	v_addc_co_u32_e32 v60, vcc, 0, v60, vcc
	v_addc_co_u32_e64 v73, s[50:51], 0, v73, s[50:51]
	s_and_b64 s[46:47], s[46:47], s[6:7]
	s_and_b64 s[40:41], s[40:41], s[6:7]
	s_nop 0
	v_addc_co_u32_e64 v60, s[46:47], 0, v60, s[46:47]
	v_addc_co_u32_e64 v73, s[40:41], 0, v73, s[40:41]
	v_readlane_b32 s48, v59, 16
	v_readlane_b32 s52, v72, 16
	s_nop 1
	v_cmp_gt_f32_e32 vcc, s48, v59
	v_cmp_gt_f32_e64 s[50:51], s52, v72
	v_cmp_eq_f32_e64 s[46:47], s48, v59
	v_cmp_eq_f32_e64 s[40:41], s52, v72
	v_addc_co_u32_e32 v60, vcc, 0, v60, vcc
	v_addc_co_u32_e64 v73, s[50:51], 0, v73, s[50:51]
	s_and_b64 s[46:47], s[46:47], s[8:9]
	s_and_b64 s[40:41], s[40:41], s[8:9]
	s_nop 0
	v_addc_co_u32_e64 v60, s[46:47], 0, v60, s[46:47]
	v_addc_co_u32_e64 v73, s[40:41], 0, v73, s[40:41]
	v_readlane_b32 s48, v59, 24
	v_readlane_b32 s52, v72, 24
	s_nop 1
	v_cmp_gt_f32_e32 vcc, s48, v59
	v_cmp_gt_f32_e64 s[50:51], s52, v72
	v_cmp_eq_f32_e64 s[46:47], s48, v59
	v_cmp_eq_f32_e64 s[40:41], s52, v72
	v_addc_co_u32_e32 v60, vcc, 0, v60, vcc
	v_addc_co_u32_e64 v73, s[50:51], 0, v73, s[50:51]
	s_and_b64 s[46:47], s[46:47], s[10:11]
	s_and_b64 s[40:41], s[40:41], s[10:11]
	s_nop 0
	v_addc_co_u32_e64 v60, s[46:47], 0, v60, s[46:47]
	v_addc_co_u32_e64 v73, s[40:41], 0, v73, s[40:41]
	v_readlane_b32 s48, v59, 32
	v_readlane_b32 s52, v72, 32
	s_nop 1
	v_cmp_gt_f32_e32 vcc, s48, v59
	v_cmp_gt_f32_e64 s[50:51], s52, v72
	v_cmp_eq_f32_e64 s[46:47], s48, v59
	v_cmp_eq_f32_e64 s[40:41], s52, v72
	v_addc_co_u32_e32 v60, vcc, 0, v60, vcc
	v_addc_co_u32_e64 v73, s[50:51], 0, v73, s[50:51]
	s_and_b64 s[46:47], s[46:47], s[12:13]
	s_and_b64 s[40:41], s[40:41], s[12:13]
	s_nop 0
; __device__ __forceinline__ void route_one(const f32x4 lg, const f32x4 rb, int lane, int& mye, float& myw) {
;     ...
;     if (rank >= 4) { c0 = c1 = c2 = c3 = -INFINITY; }
;     float wsum = 0.f; myw = 0.f; mye = 0;
; #pragma unroll
;     for (int k = 0; k < TOPK; ++k) {
;         float bv = c0; int bi = 0;
;         if (c1 > bv) { bv = c1; bi = 1; }
;         if (c2 > bv) { bv = c2; bi = 2; }
;         if (c3 > bv) { bv = c3; bi = 3; }
;         int be = lane * 4 + bi;
; #pragma unroll
;         for (int o = 1; o < 64; o <<= 1) { const float ov = __shfl_xor(bv, o); const int oe = __shfl_xor(be, o); if (ov > bv || (ov == bv && oe < be)) { bv = ov; be = oe; } }
;         float sc = 0.f;
;         if ((be >> 2) == lane) { const int b2 = be & 3; sc = b2 == 0 ? s0 : b2 == 1 ? s1 : b2 == 2 ? s2 : s3; if (b2 == 0) c0 = -INFINITY; else if (b2 == 1) c1 = -INFINITY; else if (b2 == 2) c2 = -INFINITY; else c3 = -INFINITY; }
;         sc = __shfl(sc, be >> 2);
;         wsum += sc;
;         if (lane == k) { myw = sc; mye = be; }
;     }
	v_addc_co_u32_e64 v60, s[46:47], 0, v60, s[46:47]
	v_addc_co_u32_e64 v73, s[40:41], 0, v73, s[40:41]
	v_readlane_b32 s48, v59, 40
	v_readlane_b32 s52, v72, 40
	s_nop 1
	v_cmp_gt_f32_e32 vcc, s48, v59
	v_cmp_gt_f32_e64 s[50:51], s52, v72
	v_cmp_eq_f32_e64 s[46:47], s48, v59
	v_cmp_eq_f32_e64 s[40:41], s52, v72
	v_addc_co_u32_e32 v60, vcc, 0, v60, vcc
	v_addc_co_u32_e64 v73, s[50:51], 0, v73, s[50:51]
	s_and_b64 s[46:47], s[46:47], s[14:15]
	s_and_b64 s[40:41], s[40:41], s[14:15]
	s_nop 0
	v_addc_co_u32_e64 v60, s[46:47], 0, v60, s[46:47]
	v_addc_co_u32_e64 v73, s[40:41], 0, v73, s[40:41]
	v_readlane_b32 s48, v59, 48
	v_readlane_b32 s52, v72, 48
	s_nop 1
	v_cmp_gt_f32_e32 vcc, s48, v59
	v_cmp_gt_f32_e64 s[50:51], s52, v72
	v_cmp_eq_f32_e64 s[46:47], s48, v59
	v_cmp_eq_f32_e64 s[40:41], s52, v72
	v_addc_co_u32_e32 v60, vcc, 0, v60, vcc
	v_addc_co_u32_e64 v73, s[50:51], 0, v73, s[50:51]
	s_and_b64 s[46:47], s[46:47], s[16:17]
	s_and_b64 s[40:41], s[40:41], s[16:17]
	s_nop 0
	v_addc_co_u32_e64 v60, s[46:47], 0, v60, s[46:47]
	v_addc_co_u32_e64 v73, s[40:41], 0, v73, s[40:41]
	v_readlane_b32 s48, v59, 56
	v_readlane_b32 s52, v72, 56
	s_nop 1
	v_cmp_gt_f32_e32 vcc, s48, v59
	v_cmp_gt_f32_e64 s[50:51], s52, v72
	v_cmp_eq_f32_e64 s[46:47], s48, v59
	v_cmp_eq_f32_e64 s[40:41], s52, v72
	v_addc_co_u32_e32 v60, vcc, 0, v60, vcc
	v_addc_co_u32_e64 v73, s[50:51], 0, v73, s[50:51]
	s_and_b64 s[46:47], s[46:47], s[18:19]
	s_and_b64 s[40:41], s[40:41], s[18:19]
	s_nop 0
	v_addc_co_u32_e64 v60, s[46:47], 0, v60, s[46:47]
	v_addc_co_u32_e64 v73, s[40:41], 0, v73, s[40:41]
	v_cmp_gt_u32_e32 vcc, 4, v60
	v_cmp_gt_u32_e64 s[50:51], 4, v73
	v_mov_b32_e32 v41, 0
	v_mov_b32_e32 v69, 0
	v_cndmask_b32_e32 v33, v32, v33, vcc
	v_cndmask_b32_e32 v34, v32, v34, vcc
	v_cndmask_b32_e32 v35, v32, v35, vcc
	v_cndmask_b32_e32 v36, v32, v36, vcc
	v_cndmask_b32_e64 v61, v32, v61, s[50:51]
	v_cndmask_b32_e64 v62, v32, v62, s[50:51]
	v_cndmask_b32_e64 v63, v32, v63, s[50:51]
	v_cndmask_b32_e64 v64, v32, v64, s[50:51]
	v_cmp_gt_f32_e32 vcc, v34, v33
	v_cmp_gt_f32_e64 s[50:51], v62, v61
	s_nop 0
	v_cndmask_b32_e32 v37, v33, v34, vcc
	v_cndmask_b32_e32 v39, v18, v19, vcc
	v_cndmask_b32_e64 v38, 0, 1, vcc
	v_cndmask_b32_e64 v65, v61, v62, s[50:51]
	v_cndmask_b32_e64 v67, v14, v15, s[50:51]
	v_cndmask_b32_e64 v66, 0, 1, s[50:51]
	v_cmp_gt_f32_e32 vcc, v35, v37
	v_cmp_gt_f32_e64 s[50:51], v63, v65
	s_nop 0
	v_cndmask_b32_e32 v37, v37, v35, vcc
	v_cndmask_b32_e32 v39, v39, v20, vcc
	v_cndmask_b32_e64 v38, v38, 2, vcc
	v_cndmask_b32_e64 v65, v65, v63, s[50:51]
	v_cndmask_b32_e64 v67, v67, v16, s[50:51]
	v_cndmask_b32_e64 v66, v66, 2, s[50:51]
	v_cmp_gt_f32_e32 vcc, v36, v37
	v_cmp_gt_f32_e64 s[50:51], v64, v65
	s_nop 0
	v_cndmask_b32_e32 v37, v37, v36, vcc
	v_cndmask_b32_e32 v39, v39, v21, vcc
	v_cndmask_b32_e64 v38, v38, 3, vcc
	v_cndmask_b32_e64 v65, v65, v64, s[50:51]
	v_cndmask_b32_e64 v67, v67, v17, s[50:51]
	v_cndmask_b32_e64 v66, v66, 3, s[50:51]
	v_max_f32_dpp v40, v37, v37 quad_perm:[1,0,3,2] row_mask:0xf bank_mask:0xf
	v_max_f32_dpp v68, v65, v65 quad_perm:[1,0,3,2] row_mask:0xf bank_mask:0xf
	s_nop 0
	v_max_f32_dpp v40, v40, v40 quad_perm:[2,3,0,1] row_mask:0xf bank_mask:0xf
	v_max_f32_dpp v68, v68, v68 quad_perm:[2,3,0,1] row_mask:0xf bank_mask:0xf
	s_nop 0
	v_max_f32_dpp v40, v40, v40 row_half_mirror row_mask:0xf bank_mask:0xf
	v_max_f32_dpp v68, v68, v68 row_half_mirror row_mask:0xf bank_mask:0xf
	s_nop 0
	v_max_f32_dpp v40, v40, v40 row_mirror row_mask:0xf bank_mask:0xf
	v_max_f32_dpp v68, v68, v68 row_mirror row_mask:0xf bank_mask:0xf
	s_nop 0
	v_max_f32_dpp v40, v40, v40 row_bcast:15 row_mask:0xa bank_mask:0xf
	v_max_f32_dpp v68, v68, v68 row_bcast:15 row_mask:0xa bank_mask:0xf
	s_nop 0
	v_max_f32_dpp v40, v40, v40 row_bcast:31 row_mask:0xc bank_mask:0xf
	v_max_f32_dpp v68, v68, v68 row_bcast:31 row_mask:0xc bank_mask:0xf
	s_nop 0
	v_readlane_b32 s48, v40, 63
	v_readlane_b32 s52, v68, 63
	s_nop 1
	v_cmp_eq_f32_e32 vcc, s48, v37
	v_cmp_eq_f32_e64 s[50:51], s52, v65
	s_nop 0
	s_ff1_i32_b64 s49, vcc
	s_ff1_i32_b64 s53, s[50:51]
	s_nop 0
	v_readlane_b32 s48, v38, s49
	v_readlane_b32 s33, v39, s49
	v_readlane_b32 s52, v66, s53
	v_readlane_b32 s41, v67, s53
	s_lshl2_add_u32 s48, s49, s48
	s_lshl2_add_u32 s52, s53, s52
	s_nop 0
	v_add_f32_e32 v41, s33, v41
	v_writelane_b32 v57, s48, 0
	v_writelane_b32 v58, s33, 0
	v_add_f32_e32 v69, s41, v69
	v_writelane_b32 v70, s52, 0
	v_writelane_b32 v71, s41, 0
	v_cmp_eq_u32_e32 vcc, s48, v74
	v_cmp_eq_u32_e64 s[50:51], s52, v74
	v_cmp_eq_u32_e64 s[46:47], s48, v75
	v_cmp_eq_u32_e64 s[40:41], s52, v75
	v_cndmask_b32_e32 v33, v33, v32, vcc
	v_cndmask_b32_e64 v61, v61, v32, s[50:51]
	v_cndmask_b32_e64 v34, v34, v32, s[46:47]
	v_cndmask_b32_e64 v62, v62, v32, s[40:41]
	v_cmp_eq_u32_e32 vcc, s48, v76
	v_cmp_eq_u32_e64 s[50:51], s52, v76
	v_cmp_eq_u32_e64 s[46:47], s48, v77
	v_cmp_eq_u32_e64 s[40:41], s52, v77
	v_cndmask_b32_e32 v35, v35, v32, vcc
	v_cndmask_b32_e64 v63, v63, v32, s[50:51]
	v_cndmask_b32_e64 v36, v36, v32, s[46:47]
	v_cndmask_b32_e64 v64, v64, v32, s[40:41]
	v_cmp_gt_f32_e32 vcc, v34, v33
	v_cmp_gt_f32_e64 s[50:51], v62, v61
	s_nop 0
	v_cndmask_b32_e32 v37, v33, v34, vcc
	v_cndmask_b32_e32 v39, v18, v19, vcc
	v_cndmask_b32_e64 v38, 0, 1, vcc
	v_cndmask_b32_e64 v65, v61, v62, s[50:51]
	v_cndmask_b32_e64 v67, v14, v15, s[50:51]
	v_cndmask_b32_e64 v66, 0, 1, s[50:51]
	v_cmp_gt_f32_e32 vcc, v35, v37
	v_cmp_gt_f32_e64 s[50:51], v63, v65
	s_nop 0
	v_cndmask_b32_e32 v37, v37, v35, vcc
	v_cndmask_b32_e32 v39, v39, v20, vcc
	v_cndmask_b32_e64 v38, v38, 2, vcc
	v_cndmask_b32_e64 v65, v65, v63, s[50:51]
	v_cndmask_b32_e64 v67, v67, v16, s[50:51]
; __device__ __forceinline__ void route_one(const f32x4 lg, const f32x4 rb, int lane, int& mye, float& myw) {
;     ...
; #pragma unroll
;     for (int k = 0; k < TOPK; ++k) {
;         float bv = c0; int bi = 0;
;         if (c1 > bv) { bv = c1; bi = 1; }
;         if (c2 > bv) { bv = c2; bi = 2; }
;         if (c3 > bv) { bv = c3; bi = 3; }
;         int be = lane * 4 + bi;
; #pragma unroll
;         for (int o = 1; o < 64; o <<= 1) { const float ov = __shfl_xor(bv, o); const int oe = __shfl_xor(be, o); if (ov > bv || (ov == bv && oe < be)) { bv = ov; be = oe; } }
;         float sc = 0.f;
;         if ((be >> 2) == lane) { const int b2 = be & 3; sc = b2 == 0 ? s0 : b2 == 1 ? s1 : b2 == 2 ? s2 : s3; if (b2 == 0) c0 = -INFINITY; else if (b2 == 1) c1 = -INFINITY; else if (b2 == 2) c2 = -INFINITY; else c3 = -INFINITY; }
;         sc = __shfl(sc, be >> 2);
;         wsum += sc;
;         if (lane == k) { myw = sc; mye = be; }
;     }
	v_cndmask_b32_e64 v66, v66, 2, s[50:51]
	v_cmp_gt_f32_e32 vcc, v36, v37
	v_cmp_gt_f32_e64 s[50:51], v64, v65
	s_nop 0
	v_cndmask_b32_e32 v37, v37, v36, vcc
	v_cndmask_b32_e32 v39, v39, v21, vcc
	v_cndmask_b32_e64 v38, v38, 3, vcc
	v_cndmask_b32_e64 v65, v65, v64, s[50:51]
	v_cndmask_b32_e64 v67, v67, v17, s[50:51]
	v_cndmask_b32_e64 v66, v66, 3, s[50:51]
	v_max_f32_dpp v40, v37, v37 quad_perm:[1,0,3,2] row_mask:0xf bank_mask:0xf
	v_max_f32_dpp v68, v65, v65 quad_perm:[1,0,3,2] row_mask:0xf bank_mask:0xf
	s_nop 0
	v_max_f32_dpp v40, v40, v40 quad_perm:[2,3,0,1] row_mask:0xf bank_mask:0xf
	v_max_f32_dpp v68, v68, v68 quad_perm:[2,3,0,1] row_mask:0xf bank_mask:0xf
	s_nop 0
	v_max_f32_dpp v40, v40, v40 row_half_mirror row_mask:0xf bank_mask:0xf
	v_max_f32_dpp v68, v68, v68 row_half_mirror row_mask:0xf bank_mask:0xf
	s_nop 0
	v_max_f32_dpp v40, v40, v40 row_mirror row_mask:0xf bank_mask:0xf
	v_max_f32_dpp v68, v68, v68 row_mirror row_mask:0xf bank_mask:0xf
	s_nop 0
	v_max_f32_dpp v40, v40, v40 row_bcast:15 row_mask:0xa bank_mask:0xf
	v_max_f32_dpp v68, v68, v68 row_bcast:15 row_mask:0xa bank_mask:0xf
	s_nop 0
	v_max_f32_dpp v40, v40, v40 row_bcast:31 row_mask:0xc bank_mask:0xf
	v_max_f32_dpp v68, v68, v68 row_bcast:31 row_mask:0xc bank_mask:0xf
	s_nop 0
	v_readlane_b32 s48, v40, 63
	v_readlane_b32 s52, v68, 63
	s_nop 1
	v_cmp_eq_f32_e32 vcc, s48, v37
	v_cmp_eq_f32_e64 s[50:51], s52, v65
	s_nop 0
	s_ff1_i32_b64 s49, vcc
	s_ff1_i32_b64 s53, s[50:51]
	s_nop 0
	v_readlane_b32 s48, v38, s49
	v_readlane_b32 s33, v39, s49
	v_readlane_b32 s52, v66, s53
	v_readlane_b32 s41, v67, s53
	s_lshl2_add_u32 s48, s49, s48
	s_lshl2_add_u32 s52, s53, s52
	s_nop 0
	v_add_f32_e32 v41, s33, v41
	v_writelane_b32 v57, s48, 1
	v_writelane_b32 v58, s33, 1
	v_add_f32_e32 v69, s41, v69
	v_writelane_b32 v70, s52, 1
	v_writelane_b32 v71, s41, 1
	v_cmp_eq_u32_e32 vcc, s48, v74
	v_cmp_eq_u32_e64 s[50:51], s52, v74
	v_cmp_eq_u32_e64 s[46:47], s48, v75
	v_cmp_eq_u32_e64 s[40:41], s52, v75
	v_cndmask_b32_e32 v33, v33, v32, vcc
	v_cndmask_b32_e64 v61, v61, v32, s[50:51]
	v_cndmask_b32_e64 v34, v34, v32, s[46:47]
	v_cndmask_b32_e64 v62, v62, v32, s[40:41]
	v_cmp_eq_u32_e32 vcc, s48, v76
	v_cmp_eq_u32_e64 s[50:51], s52, v76
	v_cmp_eq_u32_e64 s[46:47], s48, v77
	v_cmp_eq_u32_e64 s[40:41], s52, v77
	v_cndmask_b32_e32 v35, v35, v32, vcc
	v_cndmask_b32_e64 v63, v63, v32, s[50:51]
	v_cndmask_b32_e64 v36, v36, v32, s[46:47]
	v_cndmask_b32_e64 v64, v64, v32, s[40:41]
	v_cmp_gt_f32_e32 vcc, v34, v33
	v_cmp_gt_f32_e64 s[50:51], v62, v61
	s_nop 0
	v_cndmask_b32_e32 v37, v33, v34, vcc
	v_cndmask_b32_e32 v39, v18, v19, vcc
	v_cndmask_b32_e64 v38, 0, 1, vcc
	v_cndmask_b32_e64 v65, v61, v62, s[50:51]
	v_cndmask_b32_e64 v67, v14, v15, s[50:51]
	v_cndmask_b32_e64 v66, 0, 1, s[50:51]
	v_cmp_gt_f32_e32 vcc, v35, v37
	v_cmp_gt_f32_e64 s[50:51], v63, v65
	s_nop 0
	v_cndmask_b32_e32 v37, v37, v35, vcc
	v_cndmask_b32_e32 v39, v39, v20, vcc
	v_cndmask_b32_e64 v38, v38, 2, vcc
	v_cndmask_b32_e64 v65, v65, v63, s[50:51]
	v_cndmask_b32_e64 v67, v67, v16, s[50:51]
	v_cndmask_b32_e64 v66, v66, 2, s[50:51]
	v_cmp_gt_f32_e32 vcc, v36, v37
	v_cmp_gt_f32_e64 s[50:51], v64, v65
	s_nop 0
	v_cndmask_b32_e32 v37, v37, v36, vcc
	v_cndmask_b32_e32 v39, v39, v21, vcc
	v_cndmask_b32_e64 v38, v38, 3, vcc
	v_cndmask_b32_e64 v65, v65, v64, s[50:51]
	v_cndmask_b32_e64 v67, v67, v17, s[50:51]
	v_cndmask_b32_e64 v66, v66, 3, s[50:51]
	v_max_f32_dpp v40, v37, v37 quad_perm:[1,0,3,2] row_mask:0xf bank_mask:0xf
	v_max_f32_dpp v68, v65, v65 quad_perm:[1,0,3,2] row_mask:0xf bank_mask:0xf
	s_nop 0
	v_max_f32_dpp v40, v40, v40 quad_perm:[2,3,0,1] row_mask:0xf bank_mask:0xf
	v_max_f32_dpp v68, v68, v68 quad_perm:[2,3,0,1] row_mask:0xf bank_mask:0xf
	s_nop 0
	v_max_f32_dpp v40, v40, v40 row_half_mirror row_mask:0xf bank_mask:0xf
	v_max_f32_dpp v68, v68, v68 row_half_mirror row_mask:0xf bank_mask:0xf
	s_nop 0
	v_max_f32_dpp v40, v40, v40 row_mirror row_mask:0xf bank_mask:0xf
	v_max_f32_dpp v68, v68, v68 row_mirror row_mask:0xf bank_mask:0xf
	s_nop 0
	v_max_f32_dpp v40, v40, v40 row_bcast:15 row_mask:0xa bank_mask:0xf
	v_max_f32_dpp v68, v68, v68 row_bcast:15 row_mask:0xa bank_mask:0xf
	s_nop 0
	v_max_f32_dpp v40, v40, v40 row_bcast:31 row_mask:0xc bank_mask:0xf
	v_max_f32_dpp v68, v68, v68 row_bcast:31 row_mask:0xc bank_mask:0xf
	s_nop 0
	v_readlane_b32 s48, v40, 63
	v_readlane_b32 s52, v68, 63
	s_nop 1
	v_cmp_eq_f32_e32 vcc, s48, v37
	v_cmp_eq_f32_e64 s[50:51], s52, v65
	s_nop 0
	s_ff1_i32_b64 s49, vcc
	s_ff1_i32_b64 s53, s[50:51]
	s_nop 0
	v_readlane_b32 s48, v38, s49
	v_readlane_b32 s33, v39, s49
	v_readlane_b32 s52, v66, s53
	v_readlane_b32 s41, v67, s53
	s_lshl2_add_u32 s48, s49, s48
	s_lshl2_add_u32 s52, s53, s52
	s_nop 0
	v_add_f32_e32 v41, s33, v41
	v_writelane_b32 v57, s48, 2
	v_writelane_b32 v58, s33, 2
	v_add_f32_e32 v69, s41, v69
	v_writelane_b32 v70, s52, 2
	v_writelane_b32 v71, s41, 2
	v_cmp_eq_u32_e32 vcc, s48, v74
	v_cmp_eq_u32_e64 s[50:51], s52, v74
	v_cmp_eq_u32_e64 s[46:47], s48, v75
	v_cmp_eq_u32_e64 s[40:41], s52, v75
	v_cndmask_b32_e32 v33, v33, v32, vcc
	v_cndmask_b32_e64 v61, v61, v32, s[50:51]
	v_cndmask_b32_e64 v34, v34, v32, s[46:47]
	v_cndmask_b32_e64 v62, v62, v32, s[40:41]
	v_cmp_eq_u32_e32 vcc, s48, v76
	v_cmp_eq_u32_e64 s[50:51], s52, v76
	v_cmp_eq_u32_e64 s[46:47], s48, v77
	v_cmp_eq_u32_e64 s[40:41], s52, v77
	v_cndmask_b32_e32 v35, v35, v32, vcc
	v_cndmask_b32_e64 v63, v63, v32, s[50:51]
	v_cndmask_b32_e64 v36, v36, v32, s[46:47]
	v_cndmask_b32_e64 v64, v64, v32, s[40:41]
	v_cmp_gt_f32_e32 vcc, v34, v33
	v_cmp_gt_f32_e64 s[50:51], v62, v61
	s_nop 0
	v_cndmask_b32_e32 v37, v33, v34, vcc
; __device__ __forceinline__ void route_one(const f32x4 lg, const f32x4 rb, int lane, int& mye, float& myw) {
;     ...
; #pragma unroll
;     for (int k = 0; k < TOPK; ++k) {
;         float bv = c0; int bi = 0;
;         if (c1 > bv) { bv = c1; bi = 1; }
;         if (c2 > bv) { bv = c2; bi = 2; }
;         if (c3 > bv) { bv = c3; bi = 3; }
;         int be = lane * 4 + bi;
; #pragma unroll
;         for (int o = 1; o < 64; o <<= 1) { const float ov = __shfl_xor(bv, o); const int oe = __shfl_xor(be, o); if (ov > bv || (ov == bv && oe < be)) { bv = ov; be = oe; } }
;         float sc = 0.f;
;         if ((be >> 2) == lane) { const int b2 = be & 3; sc = b2 == 0 ? s0 : b2 == 1 ? s1 : b2 == 2 ? s2 : s3; if (b2 == 0) c0 = -INFINITY; else if (b2 == 1) c1 = -INFINITY; else if (b2 == 2) c2 = -INFINITY; else c3 = -INFINITY; }
;         sc = __shfl(sc, be >> 2);
;         wsum += sc;
;         if (lane == k) { myw = sc; mye = be; }
;     }
	v_cndmask_b32_e32 v39, v18, v19, vcc
	v_cndmask_b32_e64 v38, 0, 1, vcc
	v_cndmask_b32_e64 v65, v61, v62, s[50:51]
	v_cndmask_b32_e64 v67, v14, v15, s[50:51]
	v_cndmask_b32_e64 v66, 0, 1, s[50:51]
	v_cmp_gt_f32_e32 vcc, v35, v37
	v_cmp_gt_f32_e64 s[50:51], v63, v65
	s_nop 0
	v_cndmask_b32_e32 v37, v37, v35, vcc
	v_cndmask_b32_e32 v39, v39, v20, vcc
	v_cndmask_b32_e64 v38, v38, 2, vcc
	v_cndmask_b32_e64 v65, v65, v63, s[50:51]
	v_cndmask_b32_e64 v67, v67, v16, s[50:51]
	v_cndmask_b32_e64 v66, v66, 2, s[50:51]
	v_cmp_gt_f32_e32 vcc, v36, v37
	v_cmp_gt_f32_e64 s[50:51], v64, v65
	s_nop 0
	v_cndmask_b32_e32 v37, v37, v36, vcc
	v_cndmask_b32_e32 v39, v39, v21, vcc
	v_cndmask_b32_e64 v38, v38, 3, vcc
	v_cndmask_b32_e64 v65, v65, v64, s[50:51]
	v_cndmask_b32_e64 v67, v67, v17, s[50:51]
	v_cndmask_b32_e64 v66, v66, 3, s[50:51]
	v_max_f32_dpp v40, v37, v37 quad_perm:[1,0,3,2] row_mask:0xf bank_mask:0xf
	v_max_f32_dpp v68, v65, v65 quad_perm:[1,0,3,2] row_mask:0xf bank_mask:0xf
	s_nop 0
	v_max_f32_dpp v40, v40, v40 quad_perm:[2,3,0,1] row_mask:0xf bank_mask:0xf
	v_max_f32_dpp v68, v68, v68 quad_perm:[2,3,0,1] row_mask:0xf bank_mask:0xf
	s_nop 0
	v_max_f32_dpp v40, v40, v40 row_half_mirror row_mask:0xf bank_mask:0xf
	v_max_f32_dpp v68, v68, v68 row_half_mirror row_mask:0xf bank_mask:0xf
	s_nop 0
	v_max_f32_dpp v40, v40, v40 row_mirror row_mask:0xf bank_mask:0xf
	v_max_f32_dpp v68, v68, v68 row_mirror row_mask:0xf bank_mask:0xf
	s_nop 0
	v_max_f32_dpp v40, v40, v40 row_bcast:15 row_mask:0xa bank_mask:0xf
	v_max_f32_dpp v68, v68, v68 row_bcast:15 row_mask:0xa bank_mask:0xf
	s_nop 0
	v_max_f32_dpp v40, v40, v40 row_bcast:31 row_mask:0xc bank_mask:0xf
	v_max_f32_dpp v68, v68, v68 row_bcast:31 row_mask:0xc bank_mask:0xf
	s_nop 0
	v_readlane_b32 s48, v40, 63
	v_readlane_b32 s52, v68, 63
	s_nop 1
	v_cmp_eq_f32_e32 vcc, s48, v37
	v_cmp_eq_f32_e64 s[50:51], s52, v65
	s_nop 0
	s_ff1_i32_b64 s49, vcc
	s_ff1_i32_b64 s53, s[50:51]
	s_nop 0
	v_readlane_b32 s48, v38, s49
	v_readlane_b32 s33, v39, s49
	v_readlane_b32 s52, v66, s53
	v_readlane_b32 s41, v67, s53
	s_lshl2_add_u32 s48, s49, s48
	s_lshl2_add_u32 s52, s53, s52
	s_nop 0
	v_add_f32_e32 v41, s33, v41
	v_writelane_b32 v57, s48, 3
	v_writelane_b32 v58, s33, 3
	v_add_f32_e32 v69, s41, v69
	v_writelane_b32 v70, s52, 3
	v_writelane_b32 v71, s41, 3
	v_cmp_eq_u32_e32 vcc, s48, v74
	v_cmp_eq_u32_e64 s[50:51], s52, v74
	v_cmp_eq_u32_e64 s[46:47], s48, v75
	v_cmp_eq_u32_e64 s[40:41], s52, v75
	v_cndmask_b32_e32 v33, v33, v32, vcc
	v_cndmask_b32_e64 v61, v61, v32, s[50:51]
	v_cndmask_b32_e64 v34, v34, v32, s[46:47]
	v_cndmask_b32_e64 v62, v62, v32, s[40:41]
	v_cmp_eq_u32_e32 vcc, s48, v76
	v_cmp_eq_u32_e64 s[50:51], s52, v76
	v_cmp_eq_u32_e64 s[46:47], s48, v77
	v_cmp_eq_u32_e64 s[40:41], s52, v77
	v_cndmask_b32_e32 v35, v35, v32, vcc
	v_cndmask_b32_e64 v63, v63, v32, s[50:51]
	v_cndmask_b32_e64 v36, v36, v32, s[46:47]
	v_cndmask_b32_e64 v64, v64, v32, s[40:41]
	v_cmp_gt_f32_e32 vcc, v34, v33
	v_cmp_gt_f32_e64 s[50:51], v62, v61
	s_nop 0
	v_cndmask_b32_e32 v37, v33, v34, vcc
	v_cndmask_b32_e32 v39, v18, v19, vcc
	v_cndmask_b32_e64 v38, 0, 1, vcc
	v_cndmask_b32_e64 v65, v61, v62, s[50:51]
	v_cndmask_b32_e64 v67, v14, v15, s[50:51]
	v_cndmask_b32_e64 v66, 0, 1, s[50:51]
	v_cmp_gt_f32_e32 vcc, v35, v37
	v_cmp_gt_f32_e64 s[50:51], v63, v65
	s_nop 0
	v_cndmask_b32_e32 v37, v37, v35, vcc
	v_cndmask_b32_e32 v39, v39, v20, vcc
	v_cndmask_b32_e64 v38, v38, 2, vcc
	v_cndmask_b32_e64 v65, v65, v63, s[50:51]
	v_cndmask_b32_e64 v67, v67, v16, s[50:51]
	v_cndmask_b32_e64 v66, v66, 2, s[50:51]
	v_cmp_gt_f32_e32 vcc, v36, v37
	v_cmp_gt_f32_e64 s[50:51], v64, v65
	s_nop 0
	v_cndmask_b32_e32 v37, v37, v36, vcc
	v_cndmask_b32_e32 v39, v39, v21, vcc
	v_cndmask_b32_e64 v38, v38, 3, vcc
	v_cndmask_b32_e64 v65, v65, v64, s[50:51]
	v_cndmask_b32_e64 v67, v67, v17, s[50:51]
	v_cndmask_b32_e64 v66, v66, 3, s[50:51]
	v_max_f32_dpp v40, v37, v37 quad_perm:[1,0,3,2] row_mask:0xf bank_mask:0xf
	v_max_f32_dpp v68, v65, v65 quad_perm:[1,0,3,2] row_mask:0xf bank_mask:0xf
	s_nop 0
	v_max_f32_dpp v40, v40, v40 quad_perm:[2,3,0,1] row_mask:0xf bank_mask:0xf
	v_max_f32_dpp v68, v68, v68 quad_perm:[2,3,0,1] row_mask:0xf bank_mask:0xf
	s_nop 0
	v_max_f32_dpp v40, v40, v40 row_half_mirror row_mask:0xf bank_mask:0xf
	v_max_f32_dpp v68, v68, v68 row_half_mirror row_mask:0xf bank_mask:0xf
	s_nop 0
	v_max_f32_dpp v40, v40, v40 row_mirror row_mask:0xf bank_mask:0xf
	v_max_f32_dpp v68, v68, v68 row_mirror row_mask:0xf bank_mask:0xf
	s_nop 0
	v_max_f32_dpp v40, v40, v40 row_bcast:15 row_mask:0xa bank_mask:0xf
	v_max_f32_dpp v68, v68, v68 row_bcast:15 row_mask:0xa bank_mask:0xf
	s_nop 0
	v_max_f32_dpp v40, v40, v40 row_bcast:31 row_mask:0xc bank_mask:0xf
	v_max_f32_dpp v68, v68, v68 row_bcast:31 row_mask:0xc bank_mask:0xf
	s_nop 0
	v_readlane_b32 s48, v40, 63
	v_readlane_b32 s52, v68, 63
	s_nop 1
	v_cmp_eq_f32_e32 vcc, s48, v37
	v_cmp_eq_f32_e64 s[50:51], s52, v65
	s_nop 0
	s_ff1_i32_b64 s49, vcc
	s_ff1_i32_b64 s53, s[50:51]
	s_nop 0
	v_readlane_b32 s48, v38, s49
	v_readlane_b32 s33, v39, s49
	v_readlane_b32 s52, v66, s53
	v_readlane_b32 s41, v67, s53
	s_lshl2_add_u32 s48, s49, s48
	s_lshl2_add_u32 s52, s53, s52
	s_nop 0
	v_add_f32_e32 v41, s33, v41
	v_writelane_b32 v57, s48, 4
	v_writelane_b32 v58, s33, 4
	v_add_f32_e32 v69, s41, v69
	v_writelane_b32 v70, s52, 4
	v_writelane_b32 v71, s41, 4
	v_cmp_eq_u32_e32 vcc, s48, v74
	v_cmp_eq_u32_e64 s[50:51], s52, v74
	v_cmp_eq_u32_e64 s[46:47], s48, v75
	v_cmp_eq_u32_e64 s[40:41], s52, v75
	v_cndmask_b32_e32 v33, v33, v32, vcc
	v_cndmask_b32_e64 v61, v61, v32, s[50:51]
	v_cndmask_b32_e64 v34, v34, v32, s[46:47]
; __device__ __forceinline__ void route_one(const f32x4 lg, const f32x4 rb, int lane, int& mye, float& myw) {
;     ...
; #pragma unroll
;     for (int k = 0; k < TOPK; ++k) {
;         float bv = c0; int bi = 0;
;         if (c1 > bv) { bv = c1; bi = 1; }
;         if (c2 > bv) { bv = c2; bi = 2; }
;         if (c3 > bv) { bv = c3; bi = 3; }
;         int be = lane * 4 + bi;
; #pragma unroll
;         for (int o = 1; o < 64; o <<= 1) { const float ov = __shfl_xor(bv, o); const int oe = __shfl_xor(be, o); if (ov > bv || (ov == bv && oe < be)) { bv = ov; be = oe; } }
;         float sc = 0.f;
;         if ((be >> 2) == lane) { const int b2 = be & 3; sc = b2 == 0 ? s0 : b2 == 1 ? s1 : b2 == 2 ? s2 : s3; if (b2 == 0) c0 = -INFINITY; else if (b2 == 1) c1 = -INFINITY; else if (b2 == 2) c2 = -INFINITY; else c3 = -INFINITY; }
;         sc = __shfl(sc, be >> 2);
;         wsum += sc;
;         if (lane == k) { myw = sc; mye = be; }
;     }
	v_cndmask_b32_e64 v62, v62, v32, s[40:41]
	v_cmp_eq_u32_e32 vcc, s48, v76
	v_cmp_eq_u32_e64 s[50:51], s52, v76
	v_cmp_eq_u32_e64 s[46:47], s48, v77
	v_cmp_eq_u32_e64 s[40:41], s52, v77
	v_cndmask_b32_e32 v35, v35, v32, vcc
	v_cndmask_b32_e64 v63, v63, v32, s[50:51]
	v_cndmask_b32_e64 v36, v36, v32, s[46:47]
	v_cndmask_b32_e64 v64, v64, v32, s[40:41]
	v_cmp_gt_f32_e32 vcc, v34, v33
	v_cmp_gt_f32_e64 s[50:51], v62, v61
	s_nop 0
	v_cndmask_b32_e32 v37, v33, v34, vcc
	v_cndmask_b32_e32 v39, v18, v19, vcc
	v_cndmask_b32_e64 v38, 0, 1, vcc
	v_cndmask_b32_e64 v65, v61, v62, s[50:51]
	v_cndmask_b32_e64 v67, v14, v15, s[50:51]
	v_cndmask_b32_e64 v66, 0, 1, s[50:51]
	v_cmp_gt_f32_e32 vcc, v35, v37
	v_cmp_gt_f32_e64 s[50:51], v63, v65
	s_nop 0
	v_cndmask_b32_e32 v37, v37, v35, vcc
	v_cndmask_b32_e32 v39, v39, v20, vcc
	v_cndmask_b32_e64 v38, v38, 2, vcc
	v_cndmask_b32_e64 v65, v65, v63, s[50:51]
	v_cndmask_b32_e64 v67, v67, v16, s[50:51]
	v_cndmask_b32_e64 v66, v66, 2, s[50:51]
	v_cmp_gt_f32_e32 vcc, v36, v37
	v_cmp_gt_f32_e64 s[50:51], v64, v65
	s_nop 0
	v_cndmask_b32_e32 v37, v37, v36, vcc
	v_cndmask_b32_e32 v39, v39, v21, vcc
	v_cndmask_b32_e64 v38, v38, 3, vcc
	v_cndmask_b32_e64 v65, v65, v64, s[50:51]
	v_cndmask_b32_e64 v67, v67, v17, s[50:51]
	v_cndmask_b32_e64 v66, v66, 3, s[50:51]
	v_max_f32_dpp v40, v37, v37 quad_perm:[1,0,3,2] row_mask:0xf bank_mask:0xf
	v_max_f32_dpp v68, v65, v65 quad_perm:[1,0,3,2] row_mask:0xf bank_mask:0xf
	s_nop 0
	v_max_f32_dpp v40, v40, v40 quad_perm:[2,3,0,1] row_mask:0xf bank_mask:0xf
	v_max_f32_dpp v68, v68, v68 quad_perm:[2,3,0,1] row_mask:0xf bank_mask:0xf
	s_nop 0
	v_max_f32_dpp v40, v40, v40 row_half_mirror row_mask:0xf bank_mask:0xf
	v_max_f32_dpp v68, v68, v68 row_half_mirror row_mask:0xf bank_mask:0xf
	s_nop 0
	v_max_f32_dpp v40, v40, v40 row_mirror row_mask:0xf bank_mask:0xf
	v_max_f32_dpp v68, v68, v68 row_mirror row_mask:0xf bank_mask:0xf
	s_nop 0
	v_max_f32_dpp v40, v40, v40 row_bcast:15 row_mask:0xa bank_mask:0xf
	v_max_f32_dpp v68, v68, v68 row_bcast:15 row_mask:0xa bank_mask:0xf
	s_nop 0
	v_max_f32_dpp v40, v40, v40 row_bcast:31 row_mask:0xc bank_mask:0xf
	v_max_f32_dpp v68, v68, v68 row_bcast:31 row_mask:0xc bank_mask:0xf
	s_nop 0
	v_readlane_b32 s48, v40, 63
	v_readlane_b32 s52, v68, 63
	s_nop 1
	v_cmp_eq_f32_e32 vcc, s48, v37
	v_cmp_eq_f32_e64 s[50:51], s52, v65
	s_nop 0
	s_ff1_i32_b64 s49, vcc
	s_ff1_i32_b64 s53, s[50:51]
	s_nop 0
	v_readlane_b32 s48, v38, s49
	v_readlane_b32 s33, v39, s49
	v_readlane_b32 s52, v66, s53
	v_readlane_b32 s41, v67, s53
	s_lshl2_add_u32 s48, s49, s48
	s_lshl2_add_u32 s52, s53, s52
	s_nop 0
	v_add_f32_e32 v41, s33, v41
	v_writelane_b32 v57, s48, 5
	v_writelane_b32 v58, s33, 5
	v_add_f32_e32 v69, s41, v69
	v_writelane_b32 v70, s52, 5
	v_writelane_b32 v71, s41, 5
	v_cmp_eq_u32_e32 vcc, s48, v74
	v_cmp_eq_u32_e64 s[50:51], s52, v74
	v_cmp_eq_u32_e64 s[46:47], s48, v75
	v_cmp_eq_u32_e64 s[40:41], s52, v75
	v_cndmask_b32_e32 v33, v33, v32, vcc
	v_cndmask_b32_e64 v61, v61, v32, s[50:51]
	v_cndmask_b32_e64 v34, v34, v32, s[46:47]
	v_cndmask_b32_e64 v62, v62, v32, s[40:41]
	v_cmp_eq_u32_e32 vcc, s48, v76
	v_cmp_eq_u32_e64 s[50:51], s52, v76
	v_cmp_eq_u32_e64 s[46:47], s48, v77
	v_cmp_eq_u32_e64 s[40:41], s52, v77
	v_cndmask_b32_e32 v35, v35, v32, vcc
	v_cndmask_b32_e64 v63, v63, v32, s[50:51]
	v_cndmask_b32_e64 v36, v36, v32, s[46:47]
	v_cndmask_b32_e64 v64, v64, v32, s[40:41]
	v_cmp_gt_f32_e32 vcc, v34, v33
	v_cmp_gt_f32_e64 s[50:51], v62, v61
	s_nop 0
	v_cndmask_b32_e32 v37, v33, v34, vcc
	v_cndmask_b32_e32 v39, v18, v19, vcc
	v_cndmask_b32_e64 v38, 0, 1, vcc
	v_cndmask_b32_e64 v65, v61, v62, s[50:51]
	v_cndmask_b32_e64 v67, v14, v15, s[50:51]
	v_cndmask_b32_e64 v66, 0, 1, s[50:51]
	v_cmp_gt_f32_e32 vcc, v35, v37
	v_cmp_gt_f32_e64 s[50:51], v63, v65
	s_nop 0
	v_cndmask_b32_e32 v37, v37, v35, vcc
	v_cndmask_b32_e32 v39, v39, v20, vcc
	v_cndmask_b32_e64 v38, v38, 2, vcc
	v_cndmask_b32_e64 v65, v65, v63, s[50:51]
	v_cndmask_b32_e64 v67, v67, v16, s[50:51]
	v_cndmask_b32_e64 v66, v66, 2, s[50:51]
	v_cmp_gt_f32_e32 vcc, v36, v37
	v_cmp_gt_f32_e64 s[50:51], v64, v65
	s_nop 0
	v_cndmask_b32_e32 v37, v37, v36, vcc
	v_cndmask_b32_e32 v39, v39, v21, vcc
	v_cndmask_b32_e64 v38, v38, 3, vcc
	v_cndmask_b32_e64 v65, v65, v64, s[50:51]
	v_cndmask_b32_e64 v67, v67, v17, s[50:51]
	v_cndmask_b32_e64 v66, v66, 3, s[50:51]
	v_max_f32_dpp v40, v37, v37 quad_perm:[1,0,3,2] row_mask:0xf bank_mask:0xf
	v_max_f32_dpp v68, v65, v65 quad_perm:[1,0,3,2] row_mask:0xf bank_mask:0xf
	s_nop 0
	v_max_f32_dpp v40, v40, v40 quad_perm:[2,3,0,1] row_mask:0xf bank_mask:0xf
	v_max_f32_dpp v68, v68, v68 quad_perm:[2,3,0,1] row_mask:0xf bank_mask:0xf
	s_nop 0
	v_max_f32_dpp v40, v40, v40 row_half_mirror row_mask:0xf bank_mask:0xf
	v_max_f32_dpp v68, v68, v68 row_half_mirror row_mask:0xf bank_mask:0xf
	s_nop 0
	v_max_f32_dpp v40, v40, v40 row_mirror row_mask:0xf bank_mask:0xf
	v_max_f32_dpp v68, v68, v68 row_mirror row_mask:0xf bank_mask:0xf
	s_nop 0
	v_max_f32_dpp v40, v40, v40 row_bcast:15 row_mask:0xa bank_mask:0xf
	v_max_f32_dpp v68, v68, v68 row_bcast:15 row_mask:0xa bank_mask:0xf
	s_nop 0
	v_max_f32_dpp v40, v40, v40 row_bcast:31 row_mask:0xc bank_mask:0xf
	v_max_f32_dpp v68, v68, v68 row_bcast:31 row_mask:0xc bank_mask:0xf
	s_nop 0
	v_readlane_b32 s48, v40, 63
	v_readlane_b32 s52, v68, 63
	s_nop 1
	v_cmp_eq_f32_e32 vcc, s48, v37
	v_cmp_eq_f32_e64 s[50:51], s52, v65
	s_nop 0
	s_ff1_i32_b64 s49, vcc
	s_ff1_i32_b64 s53, s[50:51]
	s_nop 0
	v_readlane_b32 s48, v38, s49
; __device__ __forceinline__ void route_one(const f32x4 lg, const f32x4 rb, int lane, int& mye, float& myw) {
;     ...
;         if ((be >> 2) == lane) { const int b2 = be & 3; sc = b2 == 0 ? s0 : b2 == 1 ? s1 : b2 == 2 ? s2 : s3; if (b2 == 0) c0 = -INFINITY; else if (b2 == 1) c1 = -INFINITY; else if (b2 == 2) c2 = -INFINITY; else c3 = -INFINITY; }
;         sc = __shfl(sc, be >> 2);
;         wsum += sc;
;         if (lane == k) { myw = sc; mye = be; }
;     }
;     myw = myw / wsum * 2.5f;
; __device__ __forceinline__ void route_phase(const Frame& F, const float* LOGITS, const float* rbias, int* TOPE, float* TOPW, int* APOS, int* HIST, LAS int* lcnt) {
;     ...
;         if (lane < TOPK) { const int aidx = t * TOPK + lane; TOPE[aidx] = eA; TOPW[aidx] = wA; APOS[aidx] = __hip_atomic_fetch_add(lcnt + eA, 1, __ATOMIC_RELAXED, __HIP_MEMORY_SCOPE_WORKGROUP);
;             if (tB < tend) { const int bidx = tB * TOPK + lane; TOPE[bidx] = eB; TOPW[bidx] = wB; APOS[bidx] = __hip_atomic_fetch_add(lcnt + eB, 1, __ATOMIC_RELAXED, __HIP_MEMORY_SCOPE_WORKGROUP); } }
	v_readlane_b32 s33, v39, s49
	v_readlane_b32 s52, v66, s53
	v_readlane_b32 s41, v67, s53
	s_lshl2_add_u32 s48, s49, s48
	s_lshl2_add_u32 s52, s53, s52
	s_nop 0
	v_add_f32_e32 v41, s33, v41
	v_writelane_b32 v57, s48, 6
	v_writelane_b32 v58, s33, 6
	v_add_f32_e32 v69, s41, v69
	v_writelane_b32 v70, s52, 6
	v_writelane_b32 v71, s41, 6
	v_cmp_eq_u32_e32 vcc, s48, v74
	v_cmp_eq_u32_e64 s[50:51], s52, v74
	v_cmp_eq_u32_e64 s[46:47], s48, v75
	v_cmp_eq_u32_e64 s[40:41], s52, v75
	v_cndmask_b32_e32 v33, v33, v32, vcc
	v_cndmask_b32_e64 v61, v61, v32, s[50:51]
	v_cndmask_b32_e64 v34, v34, v32, s[46:47]
	v_cndmask_b32_e64 v62, v62, v32, s[40:41]
	v_cmp_eq_u32_e32 vcc, s48, v76
	v_cmp_eq_u32_e64 s[50:51], s52, v76
	v_cmp_eq_u32_e64 s[46:47], s48, v77
	v_cmp_eq_u32_e64 s[40:41], s52, v77
	v_cndmask_b32_e32 v35, v35, v32, vcc
	v_cndmask_b32_e64 v63, v63, v32, s[50:51]
	v_cndmask_b32_e64 v36, v36, v32, s[46:47]
	v_cndmask_b32_e64 v64, v64, v32, s[40:41]
	v_cmp_gt_f32_e32 vcc, v34, v33
	v_cmp_gt_f32_e64 s[50:51], v62, v61
	s_nop 0
	v_cndmask_b32_e32 v37, v33, v34, vcc
	v_cndmask_b32_e32 v39, v18, v19, vcc
	v_cndmask_b32_e64 v38, 0, 1, vcc
	v_cndmask_b32_e64 v65, v61, v62, s[50:51]
	v_cndmask_b32_e64 v67, v14, v15, s[50:51]
	v_cndmask_b32_e64 v66, 0, 1, s[50:51]
	v_cmp_gt_f32_e32 vcc, v35, v37
	v_cmp_gt_f32_e64 s[50:51], v63, v65
	s_nop 0
	v_cndmask_b32_e32 v37, v37, v35, vcc
	v_cndmask_b32_e32 v39, v39, v20, vcc
	v_cndmask_b32_e64 v38, v38, 2, vcc
	v_cndmask_b32_e64 v65, v65, v63, s[50:51]
	v_cndmask_b32_e64 v67, v67, v16, s[50:51]
	v_cndmask_b32_e64 v66, v66, 2, s[50:51]
	v_cmp_gt_f32_e32 vcc, v36, v37
	v_cmp_gt_f32_e64 s[50:51], v64, v65
	s_nop 0
	v_cndmask_b32_e32 v37, v37, v36, vcc
	v_cndmask_b32_e32 v39, v39, v21, vcc
	v_cndmask_b32_e64 v38, v38, 3, vcc
	v_cndmask_b32_e64 v65, v65, v64, s[50:51]
	v_cndmask_b32_e64 v67, v67, v17, s[50:51]
	v_cndmask_b32_e64 v66, v66, 3, s[50:51]
	v_max_f32_dpp v40, v37, v37 quad_perm:[1,0,3,2] row_mask:0xf bank_mask:0xf
	v_max_f32_dpp v68, v65, v65 quad_perm:[1,0,3,2] row_mask:0xf bank_mask:0xf
	s_nop 0
	v_max_f32_dpp v40, v40, v40 quad_perm:[2,3,0,1] row_mask:0xf bank_mask:0xf
	v_max_f32_dpp v68, v68, v68 quad_perm:[2,3,0,1] row_mask:0xf bank_mask:0xf
	s_nop 0
	v_max_f32_dpp v40, v40, v40 row_half_mirror row_mask:0xf bank_mask:0xf
	v_max_f32_dpp v68, v68, v68 row_half_mirror row_mask:0xf bank_mask:0xf
	s_nop 0
	v_max_f32_dpp v40, v40, v40 row_mirror row_mask:0xf bank_mask:0xf
	v_max_f32_dpp v68, v68, v68 row_mirror row_mask:0xf bank_mask:0xf
	s_nop 0
	v_max_f32_dpp v40, v40, v40 row_bcast:15 row_mask:0xa bank_mask:0xf
	v_max_f32_dpp v68, v68, v68 row_bcast:15 row_mask:0xa bank_mask:0xf
	s_nop 0
	v_max_f32_dpp v40, v40, v40 row_bcast:31 row_mask:0xc bank_mask:0xf
	v_max_f32_dpp v68, v68, v68 row_bcast:31 row_mask:0xc bank_mask:0xf
	s_nop 0
	v_readlane_b32 s48, v40, 63
	v_readlane_b32 s52, v68, 63
	s_nop 1
	v_cmp_eq_f32_e32 vcc, s48, v37
	v_cmp_eq_f32_e64 s[50:51], s52, v65
	s_nop 0
	s_ff1_i32_b64 s49, vcc
	s_ff1_i32_b64 s53, s[50:51]
	s_nop 0
	v_readlane_b32 s48, v38, s49
	v_readlane_b32 s33, v39, s49
	v_readlane_b32 s52, v66, s53
	v_readlane_b32 s41, v67, s53
	s_lshl2_add_u32 s48, s49, s48
	s_lshl2_add_u32 s52, s53, s52
	s_nop 0
	v_add_f32_e32 v41, s33, v41
	v_writelane_b32 v57, s48, 7
	v_writelane_b32 v58, s33, 7
	v_add_f32_e32 v69, s41, v69
	v_writelane_b32 v70, s52, 7
	v_writelane_b32 v71, s41, 7
	s_mov_b64 exec, 0xff
	v_div_scale_f32 v33, s[50:51], v41, v41, v58
	v_div_scale_f32 v35, vcc, v58, v41, v58
	v_rcp_f32_e32 v34, v33
	s_nop 0
	v_fma_f32 v36, -v33, v34, 1.0
	v_fmac_f32_e32 v34, v36, v34
	v_mul_f32_e32 v36, v35, v34
	v_fma_f32 v59, -v33, v36, v35
	v_fmac_f32_e32 v36, v59, v34
	v_fma_f32 v33, -v33, v36, v35
	v_div_fmas_f32 v33, v33, v34, v36
	v_div_fixup_f32 v59, v33, v41, v58
	v_mul_f32_e32 v59, 0x40200000, v59
	v_div_scale_f32 v61, s[50:51], v69, v69, v71
	v_div_scale_f32 v63, vcc, v71, v69, v71
	v_rcp_f32_e32 v62, v61
	s_nop 0
	v_fma_f32 v64, -v61, v62, 1.0
	v_fmac_f32_e32 v62, v64, v62
	v_mul_f32_e32 v64, v63, v62
	v_fma_f32 v72, -v61, v64, v63
	v_fmac_f32_e32 v64, v72, v62
	v_fma_f32 v61, -v61, v64, v63
	v_div_fmas_f32 v61, v61, v62, v64
	v_div_fixup_f32 v72, v61, v69, v71
	v_mul_f32_e32 v72, 0x40200000, v72
	v_ashrrev_i32_e32 v29, 31, v28
	v_add_u32_e32 v14, 64, v28
	v_lshlrev_b64 v[16:17], 2, v[28:29]
	v_ashrrev_i32_e32 v15, 31, v14
	v_lshlrev_b64 v[14:15], 2, v[14:15]
	v_readlane_b32 s46, v253, 41
	v_readlane_b32 s47, v253, 42
	v_lshlrev_b32_e32 v37, 2, v57
	v_lshlrev_b32_e32 v38, 2, v70
	v_add_u32_e32 v37, 0x20800, v37
	v_add_u32_e32 v38, 0x20800, v38
	v_lshl_add_u64 v[18:19], s[46:47], 0, v[16:17]
	v_lshl_add_u64 v[20:21], s[46:47], 0, v[14:15]
	v_readlane_b32 s46, v253, 39
	v_readlane_b32 s47, v253, 40
	global_store_dword v[18:19], v57, off
	ds_add_rtn_u32 v37, v37, v56
	s_nop 0
	v_lshl_add_u64 v[18:19], s[46:47], 0, v[16:17]
	v_lshl_add_u64 v[34:35], s[46:47], 0, v[14:15]
	v_readlane_b32 s46, v253, 44
	v_readlane_b32 s47, v253, 45
	global_store_dword v[18:19], v59, off
	s_nop 1
	v_lshl_add_u64 v[16:17], s[46:47], 0, v[16:17]
	v_lshl_add_u64 v[14:15], s[46:47], 0, v[14:15]
	s_waitcnt lgkmcnt(0)
	global_store_dword v[16:17], v37, off
	s_add_i32 s33, s44, -16
	s_cmp_ge_i32 s33, s54
	s_cbranch_scc1 .Lrt0_skipB
	global_store_dword v[20:21], v70, off
	global_store_dword v[34:35], v72, off
	ds_add_rtn_u32 v38, v38, v56
	s_waitcnt lgkmcnt(0)
	global_store_dword v[14:15], v38, off
.Lrt0_skipB:
	s_mov_b64 exec, -1
	s_branch .LBB0_1478

; __device__ __forceinline__ void route_one(const f32x4 lg, const f32x4 rb, int lane, int& mye, float& myw) {
;     const float s0 = __builtin_amdgcn_rcpf(1.f + __expf(-lg[0])), s1 = __builtin_amdgcn_rcpf(1.f + __expf(-lg[1])), s2 = __builtin_amdgcn_rcpf(1.f + __expf(-lg[2])), s3 = __builtin_amdgcn_rcpf(1.f + __expf(-lg[3]));
;     float c0 = s0 + rb[0], c1 = s1 + rb[1], c2 = s2 + rb[2], c3 = s3 + rb[3];
;     float a = fmaxf(c0, c1), bq = fminf(c0, c1);
;     { const float hi2 = fmaxf(c2, c3), lo2 = fminf(c2, c3); const float na = fmaxf(a, hi2), nb = fmaxf(fminf(a, hi2), fmaxf(bq, lo2)); a = na; bq = nb; }
; #pragma unroll
;     for (int o = 1; o < 8; o <<= 1) { const float oa = __shfl_xor(a, o), ob = __shfl_xor(bq, o); const float na = fmaxf(a, oa), nb = fmaxf(fminf(a, oa), fmaxf(bq, ob)); a = na; bq = nb; }
;     const float gs = a + bq; const int grp = lane >> 3;
;     int rank = 0;
; #pragma unroll
;     for (int j = 0; j < 8; ++j) { const float og = __shfl(gs, j * 8); rank += (og > gs || (og == gs && j < grp)) ? 1 : 0; }
.LBB0_3943:
	v_lshlrev_b32_e32 v74, 2, v1
	v_lshl_or_b32 v75, v1, 2, 1
	v_lshl_or_b32 v76, v1, 2, 2
	v_lshl_or_b32 v77, v1, 2, 3
	v_mul_f32_e32 v18, 0xbfb8aa3b, v18
	v_mul_f32_e32 v14, 0xbfb8aa3b, v14
	v_mul_f32_e32 v19, 0xbfb8aa3b, v19
	v_mul_f32_e32 v15, 0xbfb8aa3b, v15
	v_mul_f32_e32 v20, 0xbfb8aa3b, v20
	v_mul_f32_e32 v16, 0xbfb8aa3b, v16
	v_mul_f32_e32 v21, 0xbfb8aa3b, v21
	v_mul_f32_e32 v17, 0xbfb8aa3b, v17
	v_exp_f32_e32 v18, v18
	v_exp_f32_e32 v14, v14
	v_exp_f32_e32 v19, v19
	v_exp_f32_e32 v15, v15
	v_exp_f32_e32 v20, v20
	v_exp_f32_e32 v16, v16
	v_exp_f32_e32 v21, v21
	v_exp_f32_e32 v17, v17
	v_add_f32_e32 v18, 1.0, v18
	v_add_f32_e32 v14, 1.0, v14
	v_add_f32_e32 v19, 1.0, v19
	v_add_f32_e32 v15, 1.0, v15
	v_add_f32_e32 v20, 1.0, v20
	v_add_f32_e32 v16, 1.0, v16
	v_add_f32_e32 v21, 1.0, v21
	v_add_f32_e32 v17, 1.0, v17
	v_rcp_f32_e32 v18, v18
	v_rcp_f32_e32 v14, v14
	v_rcp_f32_e32 v19, v19
	v_rcp_f32_e32 v15, v15
	v_rcp_f32_e32 v20, v20
	v_rcp_f32_e32 v16, v16
	v_rcp_f32_e32 v21, v21
	v_rcp_f32_e32 v17, v17
	v_add_f32_e32 v33, v2, v18
	v_add_f32_e32 v61, v2, v14
	v_add_f32_e32 v34, v3, v19
	v_add_f32_e32 v62, v3, v15
	v_add_f32_e32 v35, v4, v20
	v_add_f32_e32 v63, v4, v16
	v_add_f32_e32 v36, v5, v21
	v_add_f32_e32 v64, v5, v17
	v_max_f32_e32 v37, v33, v34
	v_max_f32_e32 v65, v61, v62
	v_min_f32_e32 v38, v33, v34
	v_min_f32_e32 v66, v61, v62
	v_max_f32_e32 v39, v35, v36
	v_max_f32_e32 v67, v63, v64
	v_min_f32_e32 v40, v35, v36
	v_min_f32_e32 v68, v63, v64
	v_min_f32_e32 v59, v37, v39
	v_min_f32_e32 v72, v65, v67
	v_max_f32_e32 v37, v37, v39
	v_max_f32_e32 v65, v65, v67
	v_max3_f32 v38, v59, v38, v40
	v_max3_f32 v66, v72, v66, v68
	v_min_f32_dpp v40, v37, v37 quad_perm:[1,0,3,2] row_mask:0xf bank_mask:0xf
	v_min_f32_dpp v68, v65, v65 quad_perm:[1,0,3,2] row_mask:0xf bank_mask:0xf
	v_max_f32_dpp v38, v38, v38 quad_perm:[1,0,3,2] row_mask:0xf bank_mask:0xf
	v_max_f32_dpp v66, v66, v66 quad_perm:[1,0,3,2] row_mask:0xf bank_mask:0xf
	v_max_f32_dpp v37, v37, v37 quad_perm:[1,0,3,2] row_mask:0xf bank_mask:0xf
	v_max_f32_dpp v65, v65, v65 quad_perm:[1,0,3,2] row_mask:0xf bank_mask:0xf
	v_max_f32_e32 v38, v38, v40
	v_max_f32_e32 v66, v66, v68
	v_min_f32_dpp v40, v37, v37 quad_perm:[2,3,0,1] row_mask:0xf bank_mask:0xf
	v_min_f32_dpp v68, v65, v65 quad_perm:[2,3,0,1] row_mask:0xf bank_mask:0xf
	v_max_f32_dpp v38, v38, v38 quad_perm:[2,3,0,1] row_mask:0xf bank_mask:0xf
	v_max_f32_dpp v66, v66, v66 quad_perm:[2,3,0,1] row_mask:0xf bank_mask:0xf
	v_max_f32_dpp v37, v37, v37 quad_perm:[2,3,0,1] row_mask:0xf bank_mask:0xf
	v_max_f32_dpp v65, v65, v65 quad_perm:[2,3,0,1] row_mask:0xf bank_mask:0xf
	v_max_f32_e32 v38, v38, v40
	v_max_f32_e32 v66, v66, v68
	v_min_f32_dpp v40, v37, v37 row_half_mirror row_mask:0xf bank_mask:0xf
	v_min_f32_dpp v68, v65, v65 row_half_mirror row_mask:0xf bank_mask:0xf
	v_max_f32_dpp v38, v38, v38 row_half_mirror row_mask:0xf bank_mask:0xf
	v_max_f32_dpp v66, v66, v66 row_half_mirror row_mask:0xf bank_mask:0xf
	v_max_f32_dpp v37, v37, v37 row_half_mirror row_mask:0xf bank_mask:0xf
	v_max_f32_dpp v65, v65, v65 row_half_mirror row_mask:0xf bank_mask:0xf
	v_max_f32_e32 v38, v38, v40
	v_max_f32_e32 v66, v66, v68
	v_add_f32_e32 v59, v37, v38
	v_add_f32_e32 v72, v65, v66
	v_mov_b32_e32 v60, 0
	v_mov_b32_e32 v73, 0
	v_readlane_b32 s48, v59, 0
	v_readlane_b32 s52, v72, 0
	s_nop 1
	v_cmp_gt_f32_e32 vcc, s48, v59
	v_cmp_gt_f32_e64 s[50:51], s52, v72
	v_cmp_eq_f32_e64 s[46:47], s48, v59
	v_cmp_eq_f32_e64 s[40:41], s52, v72
	v_addc_co_u32_e32 v60, vcc, 0, v60, vcc
	v_addc_co_u32_e64 v73, s[50:51], 0, v73, s[50:51]
	s_and_b64 s[46:47], s[46:47], s[4:5]
	s_and_b64 s[40:41], s[40:41], s[4:5]
	s_nop 0
	v_addc_co_u32_e64 v60, s[46:47], 0, v60, s[46:47]
	v_addc_co_u32_e64 v73, s[40:41], 0, v73, s[40:41]
	v_readlane_b32 s48, v59, 8
	v_readlane_b32 s52, v72, 8
	s_nop 1
	v_cmp_gt_f32_e32 vcc, s48, v59
	v_cmp_gt_f32_e64 s[50:51], s52, v72
	v_cmp_eq_f32_e64 s[46:47], s48, v59
	v_cmp_eq_f32_e64 s[40:41], s52, v72
	v_addc_co_u32_e32 v60, vcc, 0, v60, vcc
	v_addc_co_u32_e64 v73, s[50:51], 0, v73, s[50:51]
	s_and_b64 s[46:47], s[46:47], s[6:7]
	s_and_b64 s[40:41], s[40:41], s[6:7]
	s_nop 0
	v_addc_co_u32_e64 v60, s[46:47], 0, v60, s[46:47]
	v_addc_co_u32_e64 v73, s[40:41], 0, v73, s[40:41]
	v_readlane_b32 s48, v59, 16
	v_readlane_b32 s52, v72, 16
	s_nop 1
	v_cmp_gt_f32_e32 vcc, s48, v59
	v_cmp_gt_f32_e64 s[50:51], s52, v72
	v_cmp_eq_f32_e64 s[46:47], s48, v59
	v_cmp_eq_f32_e64 s[40:41], s52, v72
	v_addc_co_u32_e32 v60, vcc, 0, v60, vcc
	v_addc_co_u32_e64 v73, s[50:51], 0, v73, s[50:51]
	s_and_b64 s[46:47], s[46:47], s[8:9]
	s_and_b64 s[40:41], s[40:41], s[8:9]
	s_nop 0
	v_addc_co_u32_e64 v60, s[46:47], 0, v60, s[46:47]
	v_addc_co_u32_e64 v73, s[40:41], 0, v73, s[40:41]
	v_readlane_b32 s48, v59, 24
	v_readlane_b32 s52, v72, 24
	s_nop 1
	v_cmp_gt_f32_e32 vcc, s48, v59
	v_cmp_gt_f32_e64 s[50:51], s52, v72
	v_cmp_eq_f32_e64 s[46:47], s48, v59
	v_cmp_eq_f32_e64 s[40:41], s52, v72
	v_addc_co_u32_e32 v60, vcc, 0, v60, vcc
	v_addc_co_u32_e64 v73, s[50:51], 0, v73, s[50:51]
	s_and_b64 s[46:47], s[46:47], s[10:11]
	s_and_b64 s[40:41], s[40:41], s[10:11]
	s_nop 0
	v_addc_co_u32_e64 v60, s[46:47], 0, v60, s[46:47]
	v_addc_co_u32_e64 v73, s[40:41], 0, v73, s[40:41]
	v_readlane_b32 s48, v59, 32
	v_readlane_b32 s52, v72, 32
	s_nop 1
	v_cmp_gt_f32_e32 vcc, s48, v59
	v_cmp_gt_f32_e64 s[50:51], s52, v72
	v_cmp_eq_f32_e64 s[46:47], s48, v59
	v_cmp_eq_f32_e64 s[40:41], s52, v72
	v_addc_co_u32_e32 v60, vcc, 0, v60, vcc
	v_addc_co_u32_e64 v73, s[50:51], 0, v73, s[50:51]
	s_and_b64 s[46:47], s[46:47], s[12:13]
	s_and_b64 s[40:41], s[40:41], s[12:13]
	s_nop 0
; __device__ __forceinline__ void route_one(const f32x4 lg, const f32x4 rb, int lane, int& mye, float& myw) {
;     ...
;     if (rank >= 4) { c0 = c1 = c2 = c3 = -INFINITY; }
;     float wsum = 0.f; myw = 0.f; mye = 0;
; #pragma unroll
;     for (int k = 0; k < TOPK; ++k) {
;         float bv = c0; int bi = 0;
;         if (c1 > bv) { bv = c1; bi = 1; }
;         if (c2 > bv) { bv = c2; bi = 2; }
;         if (c3 > bv) { bv = c3; bi = 3; }
;         int be = lane * 4 + bi;
; #pragma unroll
;         for (int o = 1; o < 64; o <<= 1) { const float ov = __shfl_xor(bv, o); const int oe = __shfl_xor(be, o); if (ov > bv || (ov == bv && oe < be)) { bv = ov; be = oe; } }
;         float sc = 0.f;
;         if ((be >> 2) == lane) { const int b2 = be & 3; sc = b2 == 0 ? s0 : b2 == 1 ? s1 : b2 == 2 ? s2 : s3; if (b2 == 0) c0 = -INFINITY; else if (b2 == 1) c1 = -INFINITY; else if (b2 == 2) c2 = -INFINITY; else c3 = -INFINITY; }
;         sc = __shfl(sc, be >> 2);
;         wsum += sc;
;         if (lane == k) { myw = sc; mye = be; }
;     }
	v_addc_co_u32_e64 v60, s[46:47], 0, v60, s[46:47]
	v_addc_co_u32_e64 v73, s[40:41], 0, v73, s[40:41]
	v_readlane_b32 s48, v59, 40
	v_readlane_b32 s52, v72, 40
	s_nop 1
	v_cmp_gt_f32_e32 vcc, s48, v59
	v_cmp_gt_f32_e64 s[50:51], s52, v72
	v_cmp_eq_f32_e64 s[46:47], s48, v59
	v_cmp_eq_f32_e64 s[40:41], s52, v72
	v_addc_co_u32_e32 v60, vcc, 0, v60, vcc
	v_addc_co_u32_e64 v73, s[50:51], 0, v73, s[50:51]
	s_and_b64 s[46:47], s[46:47], s[14:15]
	s_and_b64 s[40:41], s[40:41], s[14:15]
	s_nop 0
	v_addc_co_u32_e64 v60, s[46:47], 0, v60, s[46:47]
	v_addc_co_u32_e64 v73, s[40:41], 0, v73, s[40:41]
	v_readlane_b32 s48, v59, 48
	v_readlane_b32 s52, v72, 48
	s_nop 1
	v_cmp_gt_f32_e32 vcc, s48, v59
	v_cmp_gt_f32_e64 s[50:51], s52, v72
	v_cmp_eq_f32_e64 s[46:47], s48, v59
	v_cmp_eq_f32_e64 s[40:41], s52, v72
	v_addc_co_u32_e32 v60, vcc, 0, v60, vcc
	v_addc_co_u32_e64 v73, s[50:51], 0, v73, s[50:51]
	s_and_b64 s[46:47], s[46:47], s[16:17]
	s_and_b64 s[40:41], s[40:41], s[16:17]
	s_nop 0
	v_addc_co_u32_e64 v60, s[46:47], 0, v60, s[46:47]
	v_addc_co_u32_e64 v73, s[40:41], 0, v73, s[40:41]
	v_readlane_b32 s48, v59, 56
	v_readlane_b32 s52, v72, 56
	s_nop 1
	v_cmp_gt_f32_e32 vcc, s48, v59
	v_cmp_gt_f32_e64 s[50:51], s52, v72
	v_cmp_eq_f32_e64 s[46:47], s48, v59
	v_cmp_eq_f32_e64 s[40:41], s52, v72
	v_addc_co_u32_e32 v60, vcc, 0, v60, vcc
	v_addc_co_u32_e64 v73, s[50:51], 0, v73, s[50:51]
	s_and_b64 s[46:47], s[46:47], s[18:19]
	s_and_b64 s[40:41], s[40:41], s[18:19]
	s_nop 0
	v_addc_co_u32_e64 v60, s[46:47], 0, v60, s[46:47]
	v_addc_co_u32_e64 v73, s[40:41], 0, v73, s[40:41]
	v_cmp_gt_u32_e32 vcc, 4, v60
	v_cmp_gt_u32_e64 s[50:51], 4, v73
	v_mov_b32_e32 v41, 0
	v_mov_b32_e32 v69, 0
	v_cndmask_b32_e32 v33, v32, v33, vcc
	v_cndmask_b32_e32 v34, v32, v34, vcc
	v_cndmask_b32_e32 v35, v32, v35, vcc
	v_cndmask_b32_e32 v36, v32, v36, vcc
	v_cndmask_b32_e64 v61, v32, v61, s[50:51]
	v_cndmask_b32_e64 v62, v32, v62, s[50:51]
	v_cndmask_b32_e64 v63, v32, v63, s[50:51]
	v_cndmask_b32_e64 v64, v32, v64, s[50:51]
	v_cmp_gt_f32_e32 vcc, v34, v33
	v_cmp_gt_f32_e64 s[50:51], v62, v61
	s_nop 0
	v_cndmask_b32_e32 v37, v33, v34, vcc
	v_cndmask_b32_e32 v39, v18, v19, vcc
	v_cndmask_b32_e64 v38, 0, 1, vcc
	v_cndmask_b32_e64 v65, v61, v62, s[50:51]
	v_cndmask_b32_e64 v67, v14, v15, s[50:51]
	v_cndmask_b32_e64 v66, 0, 1, s[50:51]
	v_cmp_gt_f32_e32 vcc, v35, v37
	v_cmp_gt_f32_e64 s[50:51], v63, v65
	s_nop 0
	v_cndmask_b32_e32 v37, v37, v35, vcc
	v_cndmask_b32_e32 v39, v39, v20, vcc
	v_cndmask_b32_e64 v38, v38, 2, vcc
	v_cndmask_b32_e64 v65, v65, v63, s[50:51]
	v_cndmask_b32_e64 v67, v67, v16, s[50:51]
	v_cndmask_b32_e64 v66, v66, 2, s[50:51]
	v_cmp_gt_f32_e32 vcc, v36, v37
	v_cmp_gt_f32_e64 s[50:51], v64, v65
	s_nop 0
	v_cndmask_b32_e32 v37, v37, v36, vcc
	v_cndmask_b32_e32 v39, v39, v21, vcc
	v_cndmask_b32_e64 v38, v38, 3, vcc
	v_cndmask_b32_e64 v65, v65, v64, s[50:51]
	v_cndmask_b32_e64 v67, v67, v17, s[50:51]
	v_cndmask_b32_e64 v66, v66, 3, s[50:51]
	v_max_f32_dpp v40, v37, v37 quad_perm:[1,0,3,2] row_mask:0xf bank_mask:0xf
	v_max_f32_dpp v68, v65, v65 quad_perm:[1,0,3,2] row_mask:0xf bank_mask:0xf
	s_nop 0
	v_max_f32_dpp v40, v40, v40 quad_perm:[2,3,0,1] row_mask:0xf bank_mask:0xf
	v_max_f32_dpp v68, v68, v68 quad_perm:[2,3,0,1] row_mask:0xf bank_mask:0xf
	s_nop 0
	v_max_f32_dpp v40, v40, v40 row_half_mirror row_mask:0xf bank_mask:0xf
	v_max_f32_dpp v68, v68, v68 row_half_mirror row_mask:0xf bank_mask:0xf
	s_nop 0
	v_max_f32_dpp v40, v40, v40 row_mirror row_mask:0xf bank_mask:0xf
	v_max_f32_dpp v68, v68, v68 row_mirror row_mask:0xf bank_mask:0xf
	s_nop 0
	v_max_f32_dpp v40, v40, v40 row_bcast:15 row_mask:0xa bank_mask:0xf
	v_max_f32_dpp v68, v68, v68 row_bcast:15 row_mask:0xa bank_mask:0xf
	s_nop 0
	v_max_f32_dpp v40, v40, v40 row_bcast:31 row_mask:0xc bank_mask:0xf
	v_max_f32_dpp v68, v68, v68 row_bcast:31 row_mask:0xc bank_mask:0xf
	s_nop 0
	v_readlane_b32 s48, v40, 63
	v_readlane_b32 s52, v68, 63
	s_nop 1
	v_cmp_eq_f32_e32 vcc, s48, v37
	v_cmp_eq_f32_e64 s[50:51], s52, v65
	s_nop 0
	s_ff1_i32_b64 s49, vcc
	s_ff1_i32_b64 s53, s[50:51]
	s_nop 0
	v_readlane_b32 s48, v38, s49
	v_readlane_b32 s33, v39, s49
	v_readlane_b32 s52, v66, s53
	v_readlane_b32 s41, v67, s53
	s_lshl2_add_u32 s48, s49, s48
	s_lshl2_add_u32 s52, s53, s52
	s_nop 0
	v_add_f32_e32 v41, s33, v41
	v_writelane_b32 v57, s48, 0
	v_writelane_b32 v58, s33, 0
	v_add_f32_e32 v69, s41, v69
	v_writelane_b32 v70, s52, 0
	v_writelane_b32 v71, s41, 0
	v_cmp_eq_u32_e32 vcc, s48, v74
	v_cmp_eq_u32_e64 s[50:51], s52, v74
	v_cmp_eq_u32_e64 s[46:47], s48, v75
	v_cmp_eq_u32_e64 s[40:41], s52, v75
	v_cndmask_b32_e32 v33, v33, v32, vcc
	v_cndmask_b32_e64 v61, v61, v32, s[50:51]
	v_cndmask_b32_e64 v34, v34, v32, s[46:47]
	v_cndmask_b32_e64 v62, v62, v32, s[40:41]
	v_cmp_eq_u32_e32 vcc, s48, v76
	v_cmp_eq_u32_e64 s[50:51], s52, v76
	v_cmp_eq_u32_e64 s[46:47], s48, v77
	v_cmp_eq_u32_e64 s[40:41], s52, v77
	v_cndmask_b32_e32 v35, v35, v32, vcc
	v_cndmask_b32_e64 v63, v63, v32, s[50:51]
	v_cndmask_b32_e64 v36, v36, v32, s[46:47]
	v_cndmask_b32_e64 v64, v64, v32, s[40:41]
	v_cmp_gt_f32_e32 vcc, v34, v33
	v_cmp_gt_f32_e64 s[50:51], v62, v61
	s_nop 0
	v_cndmask_b32_e32 v37, v33, v34, vcc
	v_cndmask_b32_e32 v39, v18, v19, vcc
	v_cndmask_b32_e64 v38, 0, 1, vcc
	v_cndmask_b32_e64 v65, v61, v62, s[50:51]
	v_cndmask_b32_e64 v67, v14, v15, s[50:51]
	v_cndmask_b32_e64 v66, 0, 1, s[50:51]
	v_cmp_gt_f32_e32 vcc, v35, v37
	v_cmp_gt_f32_e64 s[50:51], v63, v65
	s_nop 0
	v_cndmask_b32_e32 v37, v37, v35, vcc
	v_cndmask_b32_e32 v39, v39, v20, vcc
	v_cndmask_b32_e64 v38, v38, 2, vcc
	v_cndmask_b32_e64 v65, v65, v63, s[50:51]
	v_cndmask_b32_e64 v67, v67, v16, s[50:51]
; __device__ __forceinline__ void route_one(const f32x4 lg, const f32x4 rb, int lane, int& mye, float& myw) {
;     ...
; #pragma unroll
;     for (int k = 0; k < TOPK; ++k) {
;         float bv = c0; int bi = 0;
;         if (c1 > bv) { bv = c1; bi = 1; }
;         if (c2 > bv) { bv = c2; bi = 2; }
;         if (c3 > bv) { bv = c3; bi = 3; }
;         int be = lane * 4 + bi;
; #pragma unroll
;         for (int o = 1; o < 64; o <<= 1) { const float ov = __shfl_xor(bv, o); const int oe = __shfl_xor(be, o); if (ov > bv || (ov == bv && oe < be)) { bv = ov; be = oe; } }
;         float sc = 0.f;
;         if ((be >> 2) == lane) { const int b2 = be & 3; sc = b2 == 0 ? s0 : b2 == 1 ? s1 : b2 == 2 ? s2 : s3; if (b2 == 0) c0 = -INFINITY; else if (b2 == 1) c1 = -INFINITY; else if (b2 == 2) c2 = -INFINITY; else c3 = -INFINITY; }
;         sc = __shfl(sc, be >> 2);
;         wsum += sc;
;         if (lane == k) { myw = sc; mye = be; }
;     }
	v_cndmask_b32_e64 v66, v66, 2, s[50:51]
	v_cmp_gt_f32_e32 vcc, v36, v37
	v_cmp_gt_f32_e64 s[50:51], v64, v65
	s_nop 0
	v_cndmask_b32_e32 v37, v37, v36, vcc
	v_cndmask_b32_e32 v39, v39, v21, vcc
	v_cndmask_b32_e64 v38, v38, 3, vcc
	v_cndmask_b32_e64 v65, v65, v64, s[50:51]
	v_cndmask_b32_e64 v67, v67, v17, s[50:51]
	v_cndmask_b32_e64 v66, v66, 3, s[50:51]
	v_max_f32_dpp v40, v37, v37 quad_perm:[1,0,3,2] row_mask:0xf bank_mask:0xf
	v_max_f32_dpp v68, v65, v65 quad_perm:[1,0,3,2] row_mask:0xf bank_mask:0xf
	s_nop 0
	v_max_f32_dpp v40, v40, v40 quad_perm:[2,3,0,1] row_mask:0xf bank_mask:0xf
	v_max_f32_dpp v68, v68, v68 quad_perm:[2,3,0,1] row_mask:0xf bank_mask:0xf
	s_nop 0
	v_max_f32_dpp v40, v40, v40 row_half_mirror row_mask:0xf bank_mask:0xf
	v_max_f32_dpp v68, v68, v68 row_half_mirror row_mask:0xf bank_mask:0xf
	s_nop 0
	v_max_f32_dpp v40, v40, v40 row_mirror row_mask:0xf bank_mask:0xf
	v_max_f32_dpp v68, v68, v68 row_mirror row_mask:0xf bank_mask:0xf
	s_nop 0
	v_max_f32_dpp v40, v40, v40 row_bcast:15 row_mask:0xa bank_mask:0xf
	v_max_f32_dpp v68, v68, v68 row_bcast:15 row_mask:0xa bank_mask:0xf
	s_nop 0
	v_max_f32_dpp v40, v40, v40 row_bcast:31 row_mask:0xc bank_mask:0xf
	v_max_f32_dpp v68, v68, v68 row_bcast:31 row_mask:0xc bank_mask:0xf
	s_nop 0
	v_readlane_b32 s48, v40, 63
	v_readlane_b32 s52, v68, 63
	s_nop 1
	v_cmp_eq_f32_e32 vcc, s48, v37
	v_cmp_eq_f32_e64 s[50:51], s52, v65
	s_nop 0
	s_ff1_i32_b64 s49, vcc
	s_ff1_i32_b64 s53, s[50:51]
	s_nop 0
	v_readlane_b32 s48, v38, s49
	v_readlane_b32 s33, v39, s49
	v_readlane_b32 s52, v66, s53
	v_readlane_b32 s41, v67, s53
	s_lshl2_add_u32 s48, s49, s48
	s_lshl2_add_u32 s52, s53, s52
	s_nop 0
	v_add_f32_e32 v41, s33, v41
	v_writelane_b32 v57, s48, 1
	v_writelane_b32 v58, s33, 1
	v_add_f32_e32 v69, s41, v69
	v_writelane_b32 v70, s52, 1
	v_writelane_b32 v71, s41, 1
	v_cmp_eq_u32_e32 vcc, s48, v74
	v_cmp_eq_u32_e64 s[50:51], s52, v74
	v_cmp_eq_u32_e64 s[46:47], s48, v75
	v_cmp_eq_u32_e64 s[40:41], s52, v75
	v_cndmask_b32_e32 v33, v33, v32, vcc
	v_cndmask_b32_e64 v61, v61, v32, s[50:51]
	v_cndmask_b32_e64 v34, v34, v32, s[46:47]
	v_cndmask_b32_e64 v62, v62, v32, s[40:41]
	v_cmp_eq_u32_e32 vcc, s48, v76
	v_cmp_eq_u32_e64 s[50:51], s52, v76
	v_cmp_eq_u32_e64 s[46:47], s48, v77
	v_cmp_eq_u32_e64 s[40:41], s52, v77
	v_cndmask_b32_e32 v35, v35, v32, vcc
	v_cndmask_b32_e64 v63, v63, v32, s[50:51]
	v_cndmask_b32_e64 v36, v36, v32, s[46:47]
	v_cndmask_b32_e64 v64, v64, v32, s[40:41]
	v_cmp_gt_f32_e32 vcc, v34, v33
	v_cmp_gt_f32_e64 s[50:51], v62, v61
	s_nop 0
	v_cndmask_b32_e32 v37, v33, v34, vcc
	v_cndmask_b32_e32 v39, v18, v19, vcc
	v_cndmask_b32_e64 v38, 0, 1, vcc
	v_cndmask_b32_e64 v65, v61, v62, s[50:51]
	v_cndmask_b32_e64 v67, v14, v15, s[50:51]
	v_cndmask_b32_e64 v66, 0, 1, s[50:51]
	v_cmp_gt_f32_e32 vcc, v35, v37
	v_cmp_gt_f32_e64 s[50:51], v63, v65
	s_nop 0
	v_cndmask_b32_e32 v37, v37, v35, vcc
	v_cndmask_b32_e32 v39, v39, v20, vcc
	v_cndmask_b32_e64 v38, v38, 2, vcc
	v_cndmask_b32_e64 v65, v65, v63, s[50:51]
	v_cndmask_b32_e64 v67, v67, v16, s[50:51]
	v_cndmask_b32_e64 v66, v66, 2, s[50:51]
	v_cmp_gt_f32_e32 vcc, v36, v37
	v_cmp_gt_f32_e64 s[50:51], v64, v65
	s_nop 0
	v_cndmask_b32_e32 v37, v37, v36, vcc
	v_cndmask_b32_e32 v39, v39, v21, vcc
	v_cndmask_b32_e64 v38, v38, 3, vcc
	v_cndmask_b32_e64 v65, v65, v64, s[50:51]
	v_cndmask_b32_e64 v67, v67, v17, s[50:51]
	v_cndmask_b32_e64 v66, v66, 3, s[50:51]
	v_max_f32_dpp v40, v37, v37 quad_perm:[1,0,3,2] row_mask:0xf bank_mask:0xf
	v_max_f32_dpp v68, v65, v65 quad_perm:[1,0,3,2] row_mask:0xf bank_mask:0xf
	s_nop 0
	v_max_f32_dpp v40, v40, v40 quad_perm:[2,3,0,1] row_mask:0xf bank_mask:0xf
	v_max_f32_dpp v68, v68, v68 quad_perm:[2,3,0,1] row_mask:0xf bank_mask:0xf
	s_nop 0
	v_max_f32_dpp v40, v40, v40 row_half_mirror row_mask:0xf bank_mask:0xf
	v_max_f32_dpp v68, v68, v68 row_half_mirror row_mask:0xf bank_mask:0xf
	s_nop 0
	v_max_f32_dpp v40, v40, v40 row_mirror row_mask:0xf bank_mask:0xf
	v_max_f32_dpp v68, v68, v68 row_mirror row_mask:0xf bank_mask:0xf
	s_nop 0
	v_max_f32_dpp v40, v40, v40 row_bcast:15 row_mask:0xa bank_mask:0xf
	v_max_f32_dpp v68, v68, v68 row_bcast:15 row_mask:0xa bank_mask:0xf
	s_nop 0
	v_max_f32_dpp v40, v40, v40 row_bcast:31 row_mask:0xc bank_mask:0xf
	v_max_f32_dpp v68, v68, v68 row_bcast:31 row_mask:0xc bank_mask:0xf
	s_nop 0
	v_readlane_b32 s48, v40, 63
	v_readlane_b32 s52, v68, 63
	s_nop 1
	v_cmp_eq_f32_e32 vcc, s48, v37
	v_cmp_eq_f32_e64 s[50:51], s52, v65
	s_nop 0
	s_ff1_i32_b64 s49, vcc
	s_ff1_i32_b64 s53, s[50:51]
	s_nop 0
	v_readlane_b32 s48, v38, s49
	v_readlane_b32 s33, v39, s49
	v_readlane_b32 s52, v66, s53
	v_readlane_b32 s41, v67, s53
	s_lshl2_add_u32 s48, s49, s48
	s_lshl2_add_u32 s52, s53, s52
	s_nop 0
	v_add_f32_e32 v41, s33, v41
	v_writelane_b32 v57, s48, 2
	v_writelane_b32 v58, s33, 2
	v_add_f32_e32 v69, s41, v69
	v_writelane_b32 v70, s52, 2
	v_writelane_b32 v71, s41, 2
	v_cmp_eq_u32_e32 vcc, s48, v74
	v_cmp_eq_u32_e64 s[50:51], s52, v74
	v_cmp_eq_u32_e64 s[46:47], s48, v75
	v_cmp_eq_u32_e64 s[40:41], s52, v75
	v_cndmask_b32_e32 v33, v33, v32, vcc
	v_cndmask_b32_e64 v61, v61, v32, s[50:51]
	v_cndmask_b32_e64 v34, v34, v32, s[46:47]
	v_cndmask_b32_e64 v62, v62, v32, s[40:41]
	v_cmp_eq_u32_e32 vcc, s48, v76
	v_cmp_eq_u32_e64 s[50:51], s52, v76
	v_cmp_eq_u32_e64 s[46:47], s48, v77
	v_cmp_eq_u32_e64 s[40:41], s52, v77
	v_cndmask_b32_e32 v35, v35, v32, vcc
	v_cndmask_b32_e64 v63, v63, v32, s[50:51]
	v_cndmask_b32_e64 v36, v36, v32, s[46:47]
	v_cndmask_b32_e64 v64, v64, v32, s[40:41]
	v_cmp_gt_f32_e32 vcc, v34, v33
	v_cmp_gt_f32_e64 s[50:51], v62, v61
	s_nop 0
	v_cndmask_b32_e32 v37, v33, v34, vcc
; __device__ __forceinline__ void route_one(const f32x4 lg, const f32x4 rb, int lane, int& mye, float& myw) {
;     ...
; #pragma unroll
;     for (int k = 0; k < TOPK; ++k) {
;         float bv = c0; int bi = 0;
;         if (c1 > bv) { bv = c1; bi = 1; }
;         if (c2 > bv) { bv = c2; bi = 2; }
;         if (c3 > bv) { bv = c3; bi = 3; }
;         int be = lane * 4 + bi;
; #pragma unroll
;         for (int o = 1; o < 64; o <<= 1) { const float ov = __shfl_xor(bv, o); const int oe = __shfl_xor(be, o); if (ov > bv || (ov == bv && oe < be)) { bv = ov; be = oe; } }
;         float sc = 0.f;
;         if ((be >> 2) == lane) { const int b2 = be & 3; sc = b2 == 0 ? s0 : b2 == 1 ? s1 : b2 == 2 ? s2 : s3; if (b2 == 0) c0 = -INFINITY; else if (b2 == 1) c1 = -INFINITY; else if (b2 == 2) c2 = -INFINITY; else c3 = -INFINITY; }
;         sc = __shfl(sc, be >> 2);
;         wsum += sc;
;         if (lane == k) { myw = sc; mye = be; }
;     }
	v_cndmask_b32_e32 v39, v18, v19, vcc
	v_cndmask_b32_e64 v38, 0, 1, vcc
	v_cndmask_b32_e64 v65, v61, v62, s[50:51]
	v_cndmask_b32_e64 v67, v14, v15, s[50:51]
	v_cndmask_b32_e64 v66, 0, 1, s[50:51]
	v_cmp_gt_f32_e32 vcc, v35, v37
	v_cmp_gt_f32_e64 s[50:51], v63, v65
	s_nop 0
	v_cndmask_b32_e32 v37, v37, v35, vcc
	v_cndmask_b32_e32 v39, v39, v20, vcc
	v_cndmask_b32_e64 v38, v38, 2, vcc
	v_cndmask_b32_e64 v65, v65, v63, s[50:51]
	v_cndmask_b32_e64 v67, v67, v16, s[50:51]
	v_cndmask_b32_e64 v66, v66, 2, s[50:51]
	v_cmp_gt_f32_e32 vcc, v36, v37
	v_cmp_gt_f32_e64 s[50:51], v64, v65
	s_nop 0
	v_cndmask_b32_e32 v37, v37, v36, vcc
	v_cndmask_b32_e32 v39, v39, v21, vcc
	v_cndmask_b32_e64 v38, v38, 3, vcc
	v_cndmask_b32_e64 v65, v65, v64, s[50:51]
	v_cndmask_b32_e64 v67, v67, v17, s[50:51]
	v_cndmask_b32_e64 v66, v66, 3, s[50:51]
	v_max_f32_dpp v40, v37, v37 quad_perm:[1,0,3,2] row_mask:0xf bank_mask:0xf
	v_max_f32_dpp v68, v65, v65 quad_perm:[1,0,3,2] row_mask:0xf bank_mask:0xf
	s_nop 0
	v_max_f32_dpp v40, v40, v40 quad_perm:[2,3,0,1] row_mask:0xf bank_mask:0xf
	v_max_f32_dpp v68, v68, v68 quad_perm:[2,3,0,1] row_mask:0xf bank_mask:0xf
	s_nop 0
	v_max_f32_dpp v40, v40, v40 row_half_mirror row_mask:0xf bank_mask:0xf
	v_max_f32_dpp v68, v68, v68 row_half_mirror row_mask:0xf bank_mask:0xf
	s_nop 0
	v_max_f32_dpp v40, v40, v40 row_mirror row_mask:0xf bank_mask:0xf
	v_max_f32_dpp v68, v68, v68 row_mirror row_mask:0xf bank_mask:0xf
	s_nop 0
	v_max_f32_dpp v40, v40, v40 row_bcast:15 row_mask:0xa bank_mask:0xf
	v_max_f32_dpp v68, v68, v68 row_bcast:15 row_mask:0xa bank_mask:0xf
	s_nop 0
	v_max_f32_dpp v40, v40, v40 row_bcast:31 row_mask:0xc bank_mask:0xf
	v_max_f32_dpp v68, v68, v68 row_bcast:31 row_mask:0xc bank_mask:0xf
	s_nop 0
	v_readlane_b32 s48, v40, 63
	v_readlane_b32 s52, v68, 63
	s_nop 1
	v_cmp_eq_f32_e32 vcc, s48, v37
	v_cmp_eq_f32_e64 s[50:51], s52, v65
	s_nop 0
	s_ff1_i32_b64 s49, vcc
	s_ff1_i32_b64 s53, s[50:51]
	s_nop 0
	v_readlane_b32 s48, v38, s49
	v_readlane_b32 s33, v39, s49
	v_readlane_b32 s52, v66, s53
	v_readlane_b32 s41, v67, s53
	s_lshl2_add_u32 s48, s49, s48
	s_lshl2_add_u32 s52, s53, s52
	s_nop 0
	v_add_f32_e32 v41, s33, v41
	v_writelane_b32 v57, s48, 3
	v_writelane_b32 v58, s33, 3
	v_add_f32_e32 v69, s41, v69
	v_writelane_b32 v70, s52, 3
	v_writelane_b32 v71, s41, 3
	v_cmp_eq_u32_e32 vcc, s48, v74
	v_cmp_eq_u32_e64 s[50:51], s52, v74
	v_cmp_eq_u32_e64 s[46:47], s48, v75
	v_cmp_eq_u32_e64 s[40:41], s52, v75
	v_cndmask_b32_e32 v33, v33, v32, vcc
	v_cndmask_b32_e64 v61, v61, v32, s[50:51]
	v_cndmask_b32_e64 v34, v34, v32, s[46:47]
	v_cndmask_b32_e64 v62, v62, v32, s[40:41]
	v_cmp_eq_u32_e32 vcc, s48, v76
	v_cmp_eq_u32_e64 s[50:51], s52, v76
	v_cmp_eq_u32_e64 s[46:47], s48, v77
	v_cmp_eq_u32_e64 s[40:41], s52, v77
	v_cndmask_b32_e32 v35, v35, v32, vcc
	v_cndmask_b32_e64 v63, v63, v32, s[50:51]
	v_cndmask_b32_e64 v36, v36, v32, s[46:47]
	v_cndmask_b32_e64 v64, v64, v32, s[40:41]
	v_cmp_gt_f32_e32 vcc, v34, v33
	v_cmp_gt_f32_e64 s[50:51], v62, v61
	s_nop 0
	v_cndmask_b32_e32 v37, v33, v34, vcc
	v_cndmask_b32_e32 v39, v18, v19, vcc
	v_cndmask_b32_e64 v38, 0, 1, vcc
	v_cndmask_b32_e64 v65, v61, v62, s[50:51]
	v_cndmask_b32_e64 v67, v14, v15, s[50:51]
	v_cndmask_b32_e64 v66, 0, 1, s[50:51]
	v_cmp_gt_f32_e32 vcc, v35, v37
	v_cmp_gt_f32_e64 s[50:51], v63, v65
	s_nop 0
	v_cndmask_b32_e32 v37, v37, v35, vcc
	v_cndmask_b32_e32 v39, v39, v20, vcc
	v_cndmask_b32_e64 v38, v38, 2, vcc
	v_cndmask_b32_e64 v65, v65, v63, s[50:51]
	v_cndmask_b32_e64 v67, v67, v16, s[50:51]
	v_cndmask_b32_e64 v66, v66, 2, s[50:51]
	v_cmp_gt_f32_e32 vcc, v36, v37
	v_cmp_gt_f32_e64 s[50:51], v64, v65
	s_nop 0
	v_cndmask_b32_e32 v37, v37, v36, vcc
	v_cndmask_b32_e32 v39, v39, v21, vcc
	v_cndmask_b32_e64 v38, v38, 3, vcc
	v_cndmask_b32_e64 v65, v65, v64, s[50:51]
	v_cndmask_b32_e64 v67, v67, v17, s[50:51]
	v_cndmask_b32_e64 v66, v66, 3, s[50:51]
	v_max_f32_dpp v40, v37, v37 quad_perm:[1,0,3,2] row_mask:0xf bank_mask:0xf
	v_max_f32_dpp v68, v65, v65 quad_perm:[1,0,3,2] row_mask:0xf bank_mask:0xf
	s_nop 0
	v_max_f32_dpp v40, v40, v40 quad_perm:[2,3,0,1] row_mask:0xf bank_mask:0xf
	v_max_f32_dpp v68, v68, v68 quad_perm:[2,3,0,1] row_mask:0xf bank_mask:0xf
	s_nop 0
	v_max_f32_dpp v40, v40, v40 row_half_mirror row_mask:0xf bank_mask:0xf
	v_max_f32_dpp v68, v68, v68 row_half_mirror row_mask:0xf bank_mask:0xf
	s_nop 0
	v_max_f32_dpp v40, v40, v40 row_mirror row_mask:0xf bank_mask:0xf
	v_max_f32_dpp v68, v68, v68 row_mirror row_mask:0xf bank_mask:0xf
	s_nop 0
	v_max_f32_dpp v40, v40, v40 row_bcast:15 row_mask:0xa bank_mask:0xf
	v_max_f32_dpp v68, v68, v68 row_bcast:15 row_mask:0xa bank_mask:0xf
	s_nop 0
	v_max_f32_dpp v40, v40, v40 row_bcast:31 row_mask:0xc bank_mask:0xf
	v_max_f32_dpp v68, v68, v68 row_bcast:31 row_mask:0xc bank_mask:0xf
	s_nop 0
	v_readlane_b32 s48, v40, 63
	v_readlane_b32 s52, v68, 63
	s_nop 1
	v_cmp_eq_f32_e32 vcc, s48, v37
	v_cmp_eq_f32_e64 s[50:51], s52, v65
	s_nop 0
	s_ff1_i32_b64 s49, vcc
	s_ff1_i32_b64 s53, s[50:51]
	s_nop 0
	v_readlane_b32 s48, v38, s49
	v_readlane_b32 s33, v39, s49
	v_readlane_b32 s52, v66, s53
	v_readlane_b32 s41, v67, s53
	s_lshl2_add_u32 s48, s49, s48
	s_lshl2_add_u32 s52, s53, s52
	s_nop 0
	v_add_f32_e32 v41, s33, v41
	v_writelane_b32 v57, s48, 4
	v_writelane_b32 v58, s33, 4
	v_add_f32_e32 v69, s41, v69
	v_writelane_b32 v70, s52, 4
	v_writelane_b32 v71, s41, 4
	v_cmp_eq_u32_e32 vcc, s48, v74
	v_cmp_eq_u32_e64 s[50:51], s52, v74
	v_cmp_eq_u32_e64 s[46:47], s48, v75
	v_cmp_eq_u32_e64 s[40:41], s52, v75
	v_cndmask_b32_e32 v33, v33, v32, vcc
	v_cndmask_b32_e64 v61, v61, v32, s[50:51]
	v_cndmask_b32_e64 v34, v34, v32, s[46:47]
; __device__ __forceinline__ void route_one(const f32x4 lg, const f32x4 rb, int lane, int& mye, float& myw) {
;     ...
; #pragma unroll
;     for (int k = 0; k < TOPK; ++k) {
;         float bv = c0; int bi = 0;
;         if (c1 > bv) { bv = c1; bi = 1; }
;         if (c2 > bv) { bv = c2; bi = 2; }
;         if (c3 > bv) { bv = c3; bi = 3; }
;         int be = lane * 4 + bi;
; #pragma unroll
;         for (int o = 1; o < 64; o <<= 1) { const float ov = __shfl_xor(bv, o); const int oe = __shfl_xor(be, o); if (ov > bv || (ov == bv && oe < be)) { bv = ov; be = oe; } }
;         float sc = 0.f;
;         if ((be >> 2) == lane) { const int b2 = be & 3; sc = b2 == 0 ? s0 : b2 == 1 ? s1 : b2 == 2 ? s2 : s3; if (b2 == 0) c0 = -INFINITY; else if (b2 == 1) c1 = -INFINITY; else if (b2 == 2) c2 = -INFINITY; else c3 = -INFINITY; }
;         sc = __shfl(sc, be >> 2);
;         wsum += sc;
;         if (lane == k) { myw = sc; mye = be; }
;     }
	v_cndmask_b32_e64 v62, v62, v32, s[40:41]
	v_cmp_eq_u32_e32 vcc, s48, v76
	v_cmp_eq_u32_e64 s[50:51], s52, v76
	v_cmp_eq_u32_e64 s[46:47], s48, v77
	v_cmp_eq_u32_e64 s[40:41], s52, v77
	v_cndmask_b32_e32 v35, v35, v32, vcc
	v_cndmask_b32_e64 v63, v63, v32, s[50:51]
	v_cndmask_b32_e64 v36, v36, v32, s[46:47]
	v_cndmask_b32_e64 v64, v64, v32, s[40:41]
	v_cmp_gt_f32_e32 vcc, v34, v33
	v_cmp_gt_f32_e64 s[50:51], v62, v61
	s_nop 0
	v_cndmask_b32_e32 v37, v33, v34, vcc
	v_cndmask_b32_e32 v39, v18, v19, vcc
	v_cndmask_b32_e64 v38, 0, 1, vcc
	v_cndmask_b32_e64 v65, v61, v62, s[50:51]
	v_cndmask_b32_e64 v67, v14, v15, s[50:51]
	v_cndmask_b32_e64 v66, 0, 1, s[50:51]
	v_cmp_gt_f32_e32 vcc, v35, v37
	v_cmp_gt_f32_e64 s[50:51], v63, v65
	s_nop 0
	v_cndmask_b32_e32 v37, v37, v35, vcc
	v_cndmask_b32_e32 v39, v39, v20, vcc
	v_cndmask_b32_e64 v38, v38, 2, vcc
	v_cndmask_b32_e64 v65, v65, v63, s[50:51]
	v_cndmask_b32_e64 v67, v67, v16, s[50:51]
	v_cndmask_b32_e64 v66, v66, 2, s[50:51]
	v_cmp_gt_f32_e32 vcc, v36, v37
	v_cmp_gt_f32_e64 s[50:51], v64, v65
	s_nop 0
	v_cndmask_b32_e32 v37, v37, v36, vcc
	v_cndmask_b32_e32 v39, v39, v21, vcc
	v_cndmask_b32_e64 v38, v38, 3, vcc
	v_cndmask_b32_e64 v65, v65, v64, s[50:51]
	v_cndmask_b32_e64 v67, v67, v17, s[50:51]
	v_cndmask_b32_e64 v66, v66, 3, s[50:51]
	v_max_f32_dpp v40, v37, v37 quad_perm:[1,0,3,2] row_mask:0xf bank_mask:0xf
	v_max_f32_dpp v68, v65, v65 quad_perm:[1,0,3,2] row_mask:0xf bank_mask:0xf
	s_nop 0
	v_max_f32_dpp v40, v40, v40 quad_perm:[2,3,0,1] row_mask:0xf bank_mask:0xf
	v_max_f32_dpp v68, v68, v68 quad_perm:[2,3,0,1] row_mask:0xf bank_mask:0xf
	s_nop 0
	v_max_f32_dpp v40, v40, v40 row_half_mirror row_mask:0xf bank_mask:0xf
	v_max_f32_dpp v68, v68, v68 row_half_mirror row_mask:0xf bank_mask:0xf
	s_nop 0
	v_max_f32_dpp v40, v40, v40 row_mirror row_mask:0xf bank_mask:0xf
	v_max_f32_dpp v68, v68, v68 row_mirror row_mask:0xf bank_mask:0xf
	s_nop 0
	v_max_f32_dpp v40, v40, v40 row_bcast:15 row_mask:0xa bank_mask:0xf
	v_max_f32_dpp v68, v68, v68 row_bcast:15 row_mask:0xa bank_mask:0xf
	s_nop 0
	v_max_f32_dpp v40, v40, v40 row_bcast:31 row_mask:0xc bank_mask:0xf
	v_max_f32_dpp v68, v68, v68 row_bcast:31 row_mask:0xc bank_mask:0xf
	s_nop 0
	v_readlane_b32 s48, v40, 63
	v_readlane_b32 s52, v68, 63
	s_nop 1
	v_cmp_eq_f32_e32 vcc, s48, v37
	v_cmp_eq_f32_e64 s[50:51], s52, v65
	s_nop 0
	s_ff1_i32_b64 s49, vcc
	s_ff1_i32_b64 s53, s[50:51]
	s_nop 0
	v_readlane_b32 s48, v38, s49
	v_readlane_b32 s33, v39, s49
	v_readlane_b32 s52, v66, s53
	v_readlane_b32 s41, v67, s53
	s_lshl2_add_u32 s48, s49, s48
	s_lshl2_add_u32 s52, s53, s52
	s_nop 0
	v_add_f32_e32 v41, s33, v41
	v_writelane_b32 v57, s48, 5
	v_writelane_b32 v58, s33, 5
	v_add_f32_e32 v69, s41, v69
	v_writelane_b32 v70, s52, 5
	v_writelane_b32 v71, s41, 5
	v_cmp_eq_u32_e32 vcc, s48, v74
	v_cmp_eq_u32_e64 s[50:51], s52, v74
	v_cmp_eq_u32_e64 s[46:47], s48, v75
	v_cmp_eq_u32_e64 s[40:41], s52, v75
	v_cndmask_b32_e32 v33, v33, v32, vcc
	v_cndmask_b32_e64 v61, v61, v32, s[50:51]
	v_cndmask_b32_e64 v34, v34, v32, s[46:47]
	v_cndmask_b32_e64 v62, v62, v32, s[40:41]
	v_cmp_eq_u32_e32 vcc, s48, v76
	v_cmp_eq_u32_e64 s[50:51], s52, v76
	v_cmp_eq_u32_e64 s[46:47], s48, v77
	v_cmp_eq_u32_e64 s[40:41], s52, v77
	v_cndmask_b32_e32 v35, v35, v32, vcc
	v_cndmask_b32_e64 v63, v63, v32, s[50:51]
	v_cndmask_b32_e64 v36, v36, v32, s[46:47]
	v_cndmask_b32_e64 v64, v64, v32, s[40:41]
	v_cmp_gt_f32_e32 vcc, v34, v33
	v_cmp_gt_f32_e64 s[50:51], v62, v61
	s_nop 0
	v_cndmask_b32_e32 v37, v33, v34, vcc
	v_cndmask_b32_e32 v39, v18, v19, vcc
	v_cndmask_b32_e64 v38, 0, 1, vcc
	v_cndmask_b32_e64 v65, v61, v62, s[50:51]
	v_cndmask_b32_e64 v67, v14, v15, s[50:51]
	v_cndmask_b32_e64 v66, 0, 1, s[50:51]
	v_cmp_gt_f32_e32 vcc, v35, v37
	v_cmp_gt_f32_e64 s[50:51], v63, v65
	s_nop 0
	v_cndmask_b32_e32 v37, v37, v35, vcc
	v_cndmask_b32_e32 v39, v39, v20, vcc
	v_cndmask_b32_e64 v38, v38, 2, vcc
	v_cndmask_b32_e64 v65, v65, v63, s[50:51]
	v_cndmask_b32_e64 v67, v67, v16, s[50:51]
	v_cndmask_b32_e64 v66, v66, 2, s[50:51]
	v_cmp_gt_f32_e32 vcc, v36, v37
	v_cmp_gt_f32_e64 s[50:51], v64, v65
	s_nop 0
	v_cndmask_b32_e32 v37, v37, v36, vcc
	v_cndmask_b32_e32 v39, v39, v21, vcc
	v_cndmask_b32_e64 v38, v38, 3, vcc
	v_cndmask_b32_e64 v65, v65, v64, s[50:51]
	v_cndmask_b32_e64 v67, v67, v17, s[50:51]
	v_cndmask_b32_e64 v66, v66, 3, s[50:51]
	v_max_f32_dpp v40, v37, v37 quad_perm:[1,0,3,2] row_mask:0xf bank_mask:0xf
	v_max_f32_dpp v68, v65, v65 quad_perm:[1,0,3,2] row_mask:0xf bank_mask:0xf
	s_nop 0
	v_max_f32_dpp v40, v40, v40 quad_perm:[2,3,0,1] row_mask:0xf bank_mask:0xf
	v_max_f32_dpp v68, v68, v68 quad_perm:[2,3,0,1] row_mask:0xf bank_mask:0xf
	s_nop 0
	v_max_f32_dpp v40, v40, v40 row_half_mirror row_mask:0xf bank_mask:0xf
	v_max_f32_dpp v68, v68, v68 row_half_mirror row_mask:0xf bank_mask:0xf
	s_nop 0
	v_max_f32_dpp v40, v40, v40 row_mirror row_mask:0xf bank_mask:0xf
	v_max_f32_dpp v68, v68, v68 row_mirror row_mask:0xf bank_mask:0xf
	s_nop 0
	v_max_f32_dpp v40, v40, v40 row_bcast:15 row_mask:0xa bank_mask:0xf
	v_max_f32_dpp v68, v68, v68 row_bcast:15 row_mask:0xa bank_mask:0xf
	s_nop 0
	v_max_f32_dpp v40, v40, v40 row_bcast:31 row_mask:0xc bank_mask:0xf
	v_max_f32_dpp v68, v68, v68 row_bcast:31 row_mask:0xc bank_mask:0xf
	s_nop 0
	v_readlane_b32 s48, v40, 63
	v_readlane_b32 s52, v68, 63
	s_nop 1
	v_cmp_eq_f32_e32 vcc, s48, v37
	v_cmp_eq_f32_e64 s[50:51], s52, v65
	s_nop 0
	s_ff1_i32_b64 s49, vcc
	s_ff1_i32_b64 s53, s[50:51]
; __device__ __forceinline__ void route_one(const f32x4 lg, const f32x4 rb, int lane, int& mye, float& myw) {
;     ...
;         if ((be >> 2) == lane) { const int b2 = be & 3; sc = b2 == 0 ? s0 : b2 == 1 ? s1 : b2 == 2 ? s2 : s3; if (b2 == 0) c0 = -INFINITY; else if (b2 == 1) c1 = -INFINITY; else if (b2 == 2) c2 = -INFINITY; else c3 = -INFINITY; }
;         sc = __shfl(sc, be >> 2);
;         wsum += sc;
;         if (lane == k) { myw = sc; mye = be; }
;     }
;     myw = myw / wsum * 2.5f;
; __device__ __forceinline__ void route_phase(const Frame& F, const float* LOGITS, const float* rbias, int* TOPE, float* TOPW, int* APOS, int* HIST, LAS int* lcnt) {
;     ...
;         if (lane < TOPK) { const int aidx = t * TOPK + lane; TOPE[aidx] = eA; TOPW[aidx] = wA; APOS[aidx] = __hip_atomic_fetch_add(lcnt + eA, 1, __ATOMIC_RELAXED, __HIP_MEMORY_SCOPE_WORKGROUP);
;             if (tB < tend) { const int bidx = tB * TOPK + lane; TOPE[bidx] = eB; TOPW[bidx] = wB; APOS[bidx] = __hip_atomic_fetch_add(lcnt + eB, 1, __ATOMIC_RELAXED, __HIP_MEMORY_SCOPE_WORKGROUP); } }
	s_nop 0
	v_readlane_b32 s48, v38, s49
	v_readlane_b32 s33, v39, s49
	v_readlane_b32 s52, v66, s53
	v_readlane_b32 s41, v67, s53
	s_lshl2_add_u32 s48, s49, s48
	s_lshl2_add_u32 s52, s53, s52
	s_nop 0
	v_add_f32_e32 v41, s33, v41
	v_writelane_b32 v57, s48, 6
	v_writelane_b32 v58, s33, 6
	v_add_f32_e32 v69, s41, v69
	v_writelane_b32 v70, s52, 6
	v_writelane_b32 v71, s41, 6
	v_cmp_eq_u32_e32 vcc, s48, v74
	v_cmp_eq_u32_e64 s[50:51], s52, v74
	v_cmp_eq_u32_e64 s[46:47], s48, v75
	v_cmp_eq_u32_e64 s[40:41], s52, v75
	v_cndmask_b32_e32 v33, v33, v32, vcc
	v_cndmask_b32_e64 v61, v61, v32, s[50:51]
	v_cndmask_b32_e64 v34, v34, v32, s[46:47]
	v_cndmask_b32_e64 v62, v62, v32, s[40:41]
	v_cmp_eq_u32_e32 vcc, s48, v76
	v_cmp_eq_u32_e64 s[50:51], s52, v76
	v_cmp_eq_u32_e64 s[46:47], s48, v77
	v_cmp_eq_u32_e64 s[40:41], s52, v77
	v_cndmask_b32_e32 v35, v35, v32, vcc
	v_cndmask_b32_e64 v63, v63, v32, s[50:51]
	v_cndmask_b32_e64 v36, v36, v32, s[46:47]
	v_cndmask_b32_e64 v64, v64, v32, s[40:41]
	v_cmp_gt_f32_e32 vcc, v34, v33
	v_cmp_gt_f32_e64 s[50:51], v62, v61
	s_nop 0
	v_cndmask_b32_e32 v37, v33, v34, vcc
	v_cndmask_b32_e32 v39, v18, v19, vcc
	v_cndmask_b32_e64 v38, 0, 1, vcc
	v_cndmask_b32_e64 v65, v61, v62, s[50:51]
	v_cndmask_b32_e64 v67, v14, v15, s[50:51]
	v_cndmask_b32_e64 v66, 0, 1, s[50:51]
	v_cmp_gt_f32_e32 vcc, v35, v37
	v_cmp_gt_f32_e64 s[50:51], v63, v65
	s_nop 0
	v_cndmask_b32_e32 v37, v37, v35, vcc
	v_cndmask_b32_e32 v39, v39, v20, vcc
	v_cndmask_b32_e64 v38, v38, 2, vcc
	v_cndmask_b32_e64 v65, v65, v63, s[50:51]
	v_cndmask_b32_e64 v67, v67, v16, s[50:51]
	v_cndmask_b32_e64 v66, v66, 2, s[50:51]
	v_cmp_gt_f32_e32 vcc, v36, v37
	v_cmp_gt_f32_e64 s[50:51], v64, v65
	s_nop 0
	v_cndmask_b32_e32 v37, v37, v36, vcc
	v_cndmask_b32_e32 v39, v39, v21, vcc
	v_cndmask_b32_e64 v38, v38, 3, vcc
	v_cndmask_b32_e64 v65, v65, v64, s[50:51]
	v_cndmask_b32_e64 v67, v67, v17, s[50:51]
	v_cndmask_b32_e64 v66, v66, 3, s[50:51]
	v_max_f32_dpp v40, v37, v37 quad_perm:[1,0,3,2] row_mask:0xf bank_mask:0xf
	v_max_f32_dpp v68, v65, v65 quad_perm:[1,0,3,2] row_mask:0xf bank_mask:0xf
	s_nop 0
	v_max_f32_dpp v40, v40, v40 quad_perm:[2,3,0,1] row_mask:0xf bank_mask:0xf
	v_max_f32_dpp v68, v68, v68 quad_perm:[2,3,0,1] row_mask:0xf bank_mask:0xf
	s_nop 0
	v_max_f32_dpp v40, v40, v40 row_half_mirror row_mask:0xf bank_mask:0xf
	v_max_f32_dpp v68, v68, v68 row_half_mirror row_mask:0xf bank_mask:0xf
	s_nop 0
	v_max_f32_dpp v40, v40, v40 row_mirror row_mask:0xf bank_mask:0xf
	v_max_f32_dpp v68, v68, v68 row_mirror row_mask:0xf bank_mask:0xf
	s_nop 0
	v_max_f32_dpp v40, v40, v40 row_bcast:15 row_mask:0xa bank_mask:0xf
	v_max_f32_dpp v68, v68, v68 row_bcast:15 row_mask:0xa bank_mask:0xf
	s_nop 0
	v_max_f32_dpp v40, v40, v40 row_bcast:31 row_mask:0xc bank_mask:0xf
	v_max_f32_dpp v68, v68, v68 row_bcast:31 row_mask:0xc bank_mask:0xf
	s_nop 0
	v_readlane_b32 s48, v40, 63
	v_readlane_b32 s52, v68, 63
	s_nop 1
	v_cmp_eq_f32_e32 vcc, s48, v37
	v_cmp_eq_f32_e64 s[50:51], s52, v65
	s_nop 0
	s_ff1_i32_b64 s49, vcc
	s_ff1_i32_b64 s53, s[50:51]
	s_nop 0
	v_readlane_b32 s48, v38, s49
	v_readlane_b32 s33, v39, s49
	v_readlane_b32 s52, v66, s53
	v_readlane_b32 s41, v67, s53
	s_lshl2_add_u32 s48, s49, s48
	s_lshl2_add_u32 s52, s53, s52
	s_nop 0
	v_add_f32_e32 v41, s33, v41
	v_writelane_b32 v57, s48, 7
	v_writelane_b32 v58, s33, 7
	v_add_f32_e32 v69, s41, v69
	v_writelane_b32 v70, s52, 7
	v_writelane_b32 v71, s41, 7
	s_mov_b64 exec, 0xff
	v_div_scale_f32 v33, s[50:51], v41, v41, v58
	v_div_scale_f32 v35, vcc, v58, v41, v58
	v_rcp_f32_e32 v34, v33
	s_nop 0
	v_fma_f32 v36, -v33, v34, 1.0
	v_fmac_f32_e32 v34, v36, v34
	v_mul_f32_e32 v36, v35, v34
	v_fma_f32 v59, -v33, v36, v35
	v_fmac_f32_e32 v36, v59, v34
	v_fma_f32 v33, -v33, v36, v35
	v_div_fmas_f32 v33, v33, v34, v36
	v_div_fixup_f32 v59, v33, v41, v58
	v_mul_f32_e32 v59, 0x40200000, v59
	v_div_scale_f32 v61, s[50:51], v69, v69, v71
	v_div_scale_f32 v63, vcc, v71, v69, v71
	v_rcp_f32_e32 v62, v61
	s_nop 0
	v_fma_f32 v64, -v61, v62, 1.0
	v_fmac_f32_e32 v62, v64, v62
	v_mul_f32_e32 v64, v63, v62
	v_fma_f32 v72, -v61, v64, v63
	v_fmac_f32_e32 v64, v72, v62
	v_fma_f32 v61, -v61, v64, v63
	v_div_fmas_f32 v61, v61, v62, v64
	v_div_fixup_f32 v72, v61, v69, v71
	v_mul_f32_e32 v72, 0x40200000, v72
	v_ashrrev_i32_e32 v29, 31, v28
	v_add_u32_e32 v14, 64, v28
	v_lshlrev_b64 v[16:17], 2, v[28:29]
	v_ashrrev_i32_e32 v15, 31, v14
	v_lshlrev_b64 v[14:15], 2, v[14:15]
	v_readlane_b32 s46, v253, 41
	v_readlane_b32 s47, v253, 42
	v_lshlrev_b32_e32 v37, 2, v57
	v_lshlrev_b32_e32 v38, 2, v70
	v_add_u32_e32 v37, 0x20800, v37
	v_add_u32_e32 v38, 0x20800, v38
	v_lshl_add_u64 v[18:19], s[46:47], 0, v[16:17]
	v_lshl_add_u64 v[20:21], s[46:47], 0, v[14:15]
	v_readlane_b32 s46, v253, 39
	v_readlane_b32 s47, v253, 40
	global_store_dword v[18:19], v57, off
	ds_add_rtn_u32 v37, v37, v56
	s_nop 0
	v_lshl_add_u64 v[18:19], s[46:47], 0, v[16:17]
	v_lshl_add_u64 v[34:35], s[46:47], 0, v[14:15]
	v_readlane_b32 s46, v253, 44
	v_readlane_b32 s47, v253, 45
	global_store_dword v[18:19], v59, off
	s_nop 1
	v_lshl_add_u64 v[16:17], s[46:47], 0, v[16:17]
	v_lshl_add_u64 v[14:15], s[46:47], 0, v[14:15]
	s_waitcnt lgkmcnt(0)
	global_store_dword v[16:17], v37, off
	s_add_i32 s33, s42, -16
	s_cmp_ge_i32 s33, s54
	s_cbranch_scc1 .Lrt1_skipB
	global_store_dword v[20:21], v70, off
	global_store_dword v[34:35], v72, off
	ds_add_rtn_u32 v38, v38, v56
	s_waitcnt lgkmcnt(0)
	global_store_dword v[14:15], v38, off
